# speedup vs baseline: 1.0504x; 1.0440x over previous
.LBB1_7:
	s_or_b64 exec, exec, s[2:3]
	v_mov_b32_e32 v10, v167
	s_waitcnt lgkmcnt(0)
	s_barrier
	s_waitcnt vmcnt(18)
	s_ashr_i32 s2, s4, 6
	s_lshl_b32 s3, s2, 3
	s_and_b32 s5, s3, 8
	s_bfe_u32 s26, s2, 0x10001
	s_or_b32 s5, s26, s5
	s_lshl_b32 s26, s2, 9
	s_and_b32 s26, s26, 0x400
	s_lshl_b32 s5, s5, 4
	s_or_b32 s28, s5, s26
	v_lshrrev_b32_e32 v182, 5, v167
	v_bfe_u32 v2, v156, 4, 1
	v_bitop3_b32 v3, v182, v156, 1 bitop3:0x78
	v_lshlrev_b32_e32 v154, 2, v182
	v_xor_b32_e32 v3, v3, v2
	v_bitop3_b32 v4, v154, v156, 4 bitop3:0x78
	v_and_b32_e32 v5, 10, v156
	v_or3_b32 v3, v5, v4, v3
	s_lshl_b32 s5, s2, 4
	v_lshlrev_b32_e32 v3, 4, v3
	s_lshl_b32 s3, s2, 13
	s_and_b32 s29, s5, 16
	v_lshlrev_b32_e32 v170, 8, v182
	v_lshl_or_b32 v171, v2, 10, v3
	s_or_b32 s26, s29, s3
	v_bitop3_b32 v179, v171, s26, v170 bitop3:0x36
	s_or_b32 s5, s26, 0x280
	v_bitop3_b32 v178, v171, s5, v170 bitop3:0x36
	s_or_b32 s30, s3, 0x800
	s_or_b32 s33, s3, 0x1000
	s_or_b32 s29, s29, 64
	s_or_b32 s34, s29, s33
	v_bitop3_b32 v180, v171, s34, v170 bitop3:0x36
	s_or_b32 s29, s3, s29
	s_or_b32 s29, s29, 0x1280
	s_and_b32 s5, s2, 1
	s_lshl_b32 s31, s5, 4
	s_or_b32 s2, s31, s3
	v_bitop3_b32 v173, v171, s2, v170 bitop3:0x36
	v_bitop3_b32 v34, v156, 31, v156 bitop3:0xc
	v_lshrrev_b32_e32 v35, 4, v34
	v_bitop3_b32 v36, v34, v182, 1 bitop3:0x6c
	v_xor_b32_e32 v36, v36, v35
	v_bitop3_b32 v34, v34, v154, 4 bitop3:0x6c
	v_bitop3_b32 v37, v156, 10, 31 bitop3:8
	v_or3_b32 v34, v37, v34, v36
	v_lshlrev_b32_e32 v35, 10, v35
	v_lshlrev_b32_e32 v34, 4, v34
	v_or3_b32 v154, v35, v34, v170
	v_bitop3_b32 v172, s2, v154, v159 bitop3:0x36
	v_bitop3_b32 v176, v171, s29, v170 bitop3:0x36
	s_or_b32 s29, s31, s30
	s_or_b32 s29, s29, 0xa0
	v_bitop3_b32 v175, v171, s29, v170 bitop3:0x36
	s_or_b32 s29, s2, 0xaa0
	s_xor_b32 s29, s29, 0x80
	v_xor_b32_e32 v174, s29, v154
	s_or_b32 s29, s26, 0x18e0
	v_bitop3_b32 v181, v171, s29, v170 bitop3:0x36
	s_or_b32 s29, s26, 0x1a60
	v_bitop3_b32 v177, v171, s29, v170 bitop3:0x36
	s_or_b32 s29, s31, 64
	s_or_b32 s3, s3, s29
	s_mov_b32 s41, s3
	s_or_b32 s29, s29, s33
	s_mov_b32 s40, s29
	s_or_b32 s3, s2, 0x18e0
	s_mov_b32 s42, s3
	s_or_b32 s2, s2, 0x1ae0
	s_xor_b32 s2, s2, 0x80
	s_mov_b32 s43, s2
	s_lshr_b32 s38, s4, 1
	v_and_b32_e32 v26, 31, v167
	v_and_b32_e32 v27, 3, v167
	v_bfe_u32 v28, v167, 3, 1
	v_bfe_u32 v29, v167, 2, 1
	v_lshl_or_b32 v27, v28, 2, v27
	v_lshl_or_b32 v27, v29, 3, v27
	v_lshlrev_b32_e32 v32, 9, v182
	v_lshl_add_u32 v30, v27, 3, v32
	v_add_u32_e32 v30, 0x10000, v30
	v_lshl_add_u32 v31, v26, 3, v32
	v_add_u32_e32 v31, 0x10400, v31
	v_xor_b32_e32 v28, 31, v26
	v_lshl_add_u32 v28, v28, 3, v32
	v_add_u32_e32 v28, 0x10400, v28
	v_bfe_u32 v29, v167, 4, 1
	v_mul_u32_u24_e32 v29, 0x78, v29
	v_xor_b32_e32 v254, s38, v29
	v_or_b32_e32 v254, 0x10800, v254
	v_and_b32_e32 v33, 16, v167
	v_cmp_eq_u32_e32 vcc, 0, v33
	ds_read2_b64 v[66:69], v30 offset0:0 offset1:32
	ds_read2_b64 v[70:73], v30 offset0:16 offset1:48
	ds_read2_b64 v[230:233], v31 offset0:0 offset1:32
	ds_read2_b64 v[234:237], v28 offset0:0 offset1:32
	ds_read2_b64 v[238:241], v254 offset0:0 offset1:16
	ds_read2_b64 v[242:245], v254 offset0:32 offset1:48
	s_waitcnt lgkmcnt(0)
	v_cndmask_b32_e32 v74, v67, v66, vcc
	v_cndmask_b32_e32 v75, v69, v68, vcc
	v_cndmask_b32_e64 v76, v66, -v67, vcc
	v_cndmask_b32_e64 v77, v68, -v69, vcc
	v_cndmask_b32_e32 v78, v71, v70, vcc
	v_cndmask_b32_e32 v79, v73, v72, vcc
	v_cndmask_b32_e64 v80, v70, -v71, vcc
	v_cndmask_b32_e64 v81, v72, -v73, vcc
	v_cvt_pk_f16_f32 v222, v74, v75
	v_cvt_pk_f16_f32 v223, v74, v75
	v_cvt_pk_f16_f32 v224, v76, v77
	v_cvt_pk_f16_f32 v225, v76, v77
	v_cvt_pk_f16_f32 v226, v78, v79
	v_cvt_pk_f16_f32 v227, v78, v79
	v_cvt_pk_f16_f32 v228, v80, v81
	v_cvt_pk_f16_f32 v229, v80, v81
	v_mul_f32_e32 v66, v231, v239
	v_mul_f32_e32 v68, v231, v238
	v_mul_f32_e32 v67, v231, v241
	v_mul_f32_e32 v69, v231, v240
	v_fma_f32 v66, v230, v238, -v66
	v_fma_f32 v68, v230, v239, v68
	v_fma_f32 v67, v230, v240, -v67
	v_fma_f32 v69, v230, v241, v69
	v_cvt_pk_f16_f32 v246, v66, v67
	v_cvt_pk_f16_f32 v248, v68, v69
	v_mul_f32_e32 v70, v233, v243
	v_mul_f32_e32 v72, v233, v242
	v_mul_f32_e32 v71, v233, v245
	v_mul_f32_e32 v73, v233, v244
	v_fma_f32 v70, v232, v242, -v70
	v_fma_f32 v72, v232, v243, v72
	v_fma_f32 v71, v232, v244, -v71
	v_fma_f32 v73, v232, v245, v73
	v_cvt_pk_f16_f32 v247, v70, v71
	v_cvt_pk_f16_f32 v249, v72, v73
	v_mul_f32_e32 v66, v235, v239
	v_mul_f32_e32 v68, v235, v238
	v_mul_f32_e32 v67, v235, v241
	v_mul_f32_e32 v69, v235, v240
	v_fma_f32 v66, v234, v238, -v66
	v_fma_f32 v68, v234, v239, v68
	v_fma_f32 v67, v234, v240, -v67
	v_fma_f32 v69, v234, v241, v69
	v_cvt_pk_f16_f32 v250, v66, v67
	v_cvt_pk_f16_f32 v252, v68, v69
	v_mul_f32_e32 v70, v237, v243
	v_mul_f32_e32 v72, v237, v242
	v_mul_f32_e32 v71, v237, v245
	v_mul_f32_e32 v73, v237, v244
	v_fma_f32 v70, v236, v242, -v70
	v_fma_f32 v72, v236, v243, v72
	v_fma_f32 v71, v236, v244, -v71
	v_fma_f32 v73, v236, v245, v73
	v_cvt_pk_f16_f32 v251, v70, v71
	v_cvt_pk_f16_f32 v253, v72, v73
	v_xor_b32_e32 v255, 8, v254
	ds_read2_b64 v[238:241], v255 offset0:0 offset1:16
	ds_read2_b64 v[242:245], v255 offset0:32 offset1:48
	v_mfma_f32_32x32x16_f16 v[2:17], v[222:225], v[246:249], 0
	v_mfma_f32_32x32x16_f16 v[18:33], v[226:229], v[250:253], 0
	s_waitcnt lgkmcnt(0)
	v_mul_f32_e32 v66, v231, v239
	v_mul_f32_e32 v68, v231, v238
	v_mul_f32_e32 v67, v231, v241
	v_mul_f32_e32 v69, v231, v240
	v_fma_f32 v66, v230, v238, -v66
	v_fma_f32 v68, v230, v239, v68
	v_fma_f32 v67, v230, v240, -v67
	v_fma_f32 v69, v230, v241, v69
	v_cvt_pk_f16_f32 v246, v66, v67
	v_cvt_pk_f16_f32 v248, v68, v69
	v_mul_f32_e32 v70, v233, v243
	v_mul_f32_e32 v72, v233, v242
	v_mul_f32_e32 v71, v233, v245
	v_mul_f32_e32 v73, v233, v244
	v_fma_f32 v70, v232, v242, -v70
	v_fma_f32 v72, v232, v243, v72
	v_fma_f32 v71, v232, v244, -v71
	v_fma_f32 v73, v232, v245, v73
	v_cvt_pk_f16_f32 v247, v70, v71
	v_cvt_pk_f16_f32 v249, v72, v73
	v_cvt_pk_f16_f32 v2, v2, v3
	v_cvt_pk_f16_f32 v3, v4, v5
	v_cvt_pk_f16_f32 v4, v6, v7
	v_cvt_pk_f16_f32 v5, v8, v9
	v_cvt_pk_f16_f32 v6, v10, v11
	v_cvt_pk_f16_f32 v7, v12, v13
	v_cvt_pk_f16_f32 v8, v14, v15
	v_cvt_pk_f16_f32 v9, v16, v17
	v_cvt_pk_f16_f32 v18, v18, v19
	v_cvt_pk_f16_f32 v19, v20, v21
	v_cvt_pk_f16_f32 v20, v22, v23
	v_cvt_pk_f16_f32 v21, v24, v25
	v_cvt_pk_f16_f32 v22, v26, v27
	v_cvt_pk_f16_f32 v23, v28, v29
	v_cvt_pk_f16_f32 v24, v30, v31
	v_cvt_pk_f16_f32 v25, v32, v33
	s_setprio 1
	s_waitcnt vmcnt(14)
	v_mul_f32_e32 v66, v235, v239
	v_mul_f32_e32 v68, v235, v238
	v_mfma_f32_32x32x16_f16 v[34:49], v[2:5], v[150:153], 0
	v_mul_f32_e32 v67, v235, v241
	v_mul_f32_e32 v69, v235, v240
	v_mfma_f32_32x32x16_f16 v[34:49], v[18:21], v[146:149], v[34:49]
	v_fma_f32 v66, v234, v238, -v66
	v_fma_f32 v68, v234, v239, v68
	v_mfma_f32_32x32x16_f16 v[34:49], v[6:9], v[142:145], v[34:49]
	v_fma_f32 v67, v234, v240, -v67
	v_fma_f32 v69, v234, v241, v69
	v_mfma_f32_32x32x16_f16 v[34:49], v[22:25], v[138:141], v[34:49]
	v_cvt_pk_f16_f32 v250, v66, v67
	v_cvt_pk_f16_f32 v252, v68, v69
	s_waitcnt vmcnt(5)
	v_mul_f32_e32 v70, v237, v243
	v_mul_f32_e32 v72, v237, v242
	v_mfma_f32_32x32x16_f16 v[50:65], v[2:5], v[134:137], 0
	v_mul_f32_e32 v71, v237, v245
	v_mul_f32_e32 v73, v237, v244
	v_mfma_f32_32x32x16_f16 v[50:65], v[18:21], v[126:129], v[50:65]
	v_fma_f32 v70, v236, v242, -v70
	v_fma_f32 v72, v236, v243, v72
	v_mfma_f32_32x32x16_f16 v[50:65], v[6:9], v[122:125], v[50:65]
	v_fma_f32 v71, v236, v244, -v71
	v_fma_f32 v73, v236, v245, v73
	v_mfma_f32_32x32x16_f16 v[50:65], v[22:25], v[130:133], v[50:65]
	v_cvt_pk_f16_f32 v251, v70, v71
	v_cvt_pk_f16_f32 v253, v72, v73
	v_xor_b32_e32 v255, 16, v254
	ds_read2_b64 v[238:241], v255 offset0:0 offset1:16
	ds_read2_b64 v[242:245], v255 offset0:32 offset1:48
	v_mfma_f32_32x32x16_f16 v[2:17], v[222:225], v[246:249], 0
	v_mfma_f32_32x32x16_f16 v[18:33], v[226:229], v[250:253], 0
	v_cvt_pk_f16_f32 v34, v34, v35
	v_cvt_pk_f16_f32 v35, v36, v37
	v_cvt_pk_f16_f32 v36, v38, v39
	v_cvt_pk_f16_f32 v37, v40, v41
	v_cvt_pk_f16_f32 v38, v42, v43
	v_cvt_pk_f16_f32 v39, v44, v45
	v_cvt_pk_f16_f32 v40, v46, v47
	v_cvt_pk_f16_f32 v41, v48, v49
	v_cvt_pk_f16_f32 v50, v50, v51
	v_cvt_pk_f16_f32 v51, v52, v53
	v_cvt_pk_f16_f32 v52, v54, v55
	v_cvt_pk_f16_f32 v53, v56, v57
	v_cvt_pk_f16_f32 v54, v58, v59
	v_cvt_pk_f16_f32 v55, v60, v61
	v_cvt_pk_f16_f32 v56, v62, v63
	v_cvt_pk_f16_f32 v57, v64, v65
	s_waitcnt vmcnt(2)
	v_cvt_pk_f16_f32 v2, v2, v3
	v_cvt_pk_f16_f32 v3, v4, v5
	v_cvt_pk_f16_f32 v4, v6, v7
	v_cvt_pk_f16_f32 v5, v8, v9
	v_mfma_f32_32x32x16_f16 v[190:205], v[34:37], v[118:121], 0
	v_cvt_pk_f16_f32 v6, v10, v11
	v_cvt_pk_f16_f32 v7, v12, v13
	v_cvt_pk_f16_f32 v8, v14, v15
	v_cvt_pk_f16_f32 v9, v16, v17
	v_mfma_f32_32x32x16_f16 v[206:221], v[34:37], v[102:105], 0
	v_cvt_pk_f16_f32 v18, v18, v19
	v_cvt_pk_f16_f32 v19, v20, v21
	v_cvt_pk_f16_f32 v20, v22, v23
	v_cvt_pk_f16_f32 v21, v24, v25
	v_mfma_f32_32x32x16_f16 v[190:205], v[38:41], v[114:117], v[190:205]
	v_cvt_pk_f16_f32 v22, v26, v27
	v_cvt_pk_f16_f32 v23, v28, v29
	v_cvt_pk_f16_f32 v24, v30, v31
	v_cvt_pk_f16_f32 v25, v32, v33
	v_mfma_f32_32x32x16_f16 v[206:221], v[38:41], v[98:101], v[206:221]
	s_waitcnt lgkmcnt(0)
	v_mul_f32_e32 v66, v231, v239
	v_mul_f32_e32 v68, v231, v238
	v_mul_f32_e32 v67, v231, v241
	v_mfma_f32_32x32x16_f16 v[190:205], v[50:53], v[110:113], v[190:205]
	v_mul_f32_e32 v69, v231, v240
	v_fma_f32 v66, v230, v238, -v66
	v_fma_f32 v68, v230, v239, v68
	v_fma_f32 v67, v230, v240, -v67
	v_mfma_f32_32x32x16_f16 v[206:221], v[50:53], v[94:97], v[206:221]
	v_fma_f32 v69, v230, v241, v69
	v_cvt_pk_f16_f32 v246, v66, v67
	v_cvt_pk_f16_f32 v248, v68, v69
	v_mul_f32_e32 v70, v233, v243
	v_mfma_f32_32x32x16_f16 v[190:205], v[54:57], v[106:109], v[190:205]
	v_mul_f32_e32 v72, v233, v242
	v_mul_f32_e32 v71, v233, v245
	v_mul_f32_e32 v73, v233, v244
	v_fma_f32 v70, v232, v242, -v70
	v_mfma_f32_32x32x16_f16 v[206:221], v[54:57], v[90:93], v[206:221]
	v_fma_f32 v72, v232, v243, v72
	v_fma_f32 v71, v232, v244, -v71
	v_fma_f32 v73, v232, v245, v73
	v_cvt_pk_f16_f32 v247, v70, v71
	v_cvt_pk_f16_f32 v249, v72, v73
	v_mfma_f32_32x32x16_f16 v[34:49], v[2:5], v[150:153], 0
	v_mul_f32_e32 v66, v235, v239
	v_mul_f32_e32 v68, v235, v238
	v_mul_f32_e32 v67, v235, v241
	v_mul_f32_e32 v69, v235, v240
	v_fma_f32 v66, v234, v238, -v66
	v_mfma_f32_32x32x16_f16 v[34:49], v[18:21], v[146:149], v[34:49]
	v_fma_f32 v68, v234, v239, v68
	v_fma_f32 v67, v234, v240, -v67
	v_fma_f32 v69, v234, v241, v69
	v_cvt_pk_f16_f32 v250, v66, v67
	v_cvt_pk_f16_f32 v252, v68, v69
	v_mfma_f32_32x32x16_f16 v[34:49], v[6:9], v[142:145], v[34:49]
	v_mul_f32_e32 v70, v237, v243
	v_mul_f32_e32 v72, v237, v242
	v_mul_f32_e32 v71, v237, v245
	v_mul_f32_e32 v73, v237, v244
	v_fma_f32 v70, v236, v242, -v70
	v_mfma_f32_32x32x16_f16 v[34:49], v[22:25], v[138:141], v[34:49]
	v_fma_f32 v72, v236, v243, v72
	v_fma_f32 v71, v236, v244, -v71
	v_fma_f32 v73, v236, v245, v73
	v_cvt_pk_f16_f32 v251, v70, v71
	v_cvt_pk_f16_f32 v253, v72, v73
	v_mfma_f32_32x32x16_f16 v[50:65], v[2:5], v[134:137], 0
	v_cvt_pk_f16_f32 v190, v190, v191
	v_cvt_pk_f16_f32 v191, v192, v193
	v_cvt_pk_f16_f32 v192, v194, v195
	v_cvt_pk_f16_f32 v193, v196, v197
	v_cvt_pk_f16_f32 v194, v198, v199
	v_mfma_f32_32x32x16_f16 v[50:65], v[18:21], v[126:129], v[50:65]
	v_cvt_pk_f16_f32 v195, v200, v201
	v_cvt_pk_f16_f32 v196, v202, v203
	v_cvt_pk_f16_f32 v197, v204, v205
	v_cvt_pk_f16_f32 v206, v206, v207
	v_cvt_pk_f16_f32 v207, v208, v209
	v_mfma_f32_32x32x16_f16 v[50:65], v[6:9], v[122:125], v[50:65]
	v_cvt_pk_f16_f32 v208, v210, v211
	v_cvt_pk_f16_f32 v209, v212, v213
	v_cvt_pk_f16_f32 v210, v214, v215
	v_cvt_pk_f16_f32 v211, v216, v217
	v_cvt_pk_f16_f32 v212, v218, v219
	v_mfma_f32_32x32x16_f16 v[50:65], v[22:25], v[130:133], v[50:65]
	v_cvt_pk_f16_f32 v213, v220, v221
	ds_write_b128 v173, v[190:193]
	ds_write_b128 v172, v[194:197]
	ds_write_b128 v173, v[206:209] offset:32768
	ds_write_b128 v172, v[210:213] offset:32768
	v_xor_b32_e32 v255, 24, v254
	ds_read2_b64 v[238:241], v255 offset0:0 offset1:16
	ds_read2_b64 v[242:245], v255 offset0:32 offset1:48
	v_mfma_f32_32x32x16_f16 v[2:17], v[222:225], v[246:249], 0
	v_mfma_f32_32x32x16_f16 v[18:33], v[226:229], v[250:253], 0
	v_cvt_pk_f16_f32 v34, v34, v35
	v_cvt_pk_f16_f32 v35, v36, v37
	v_cvt_pk_f16_f32 v36, v38, v39
	v_cvt_pk_f16_f32 v37, v40, v41
	v_cvt_pk_f16_f32 v38, v42, v43
	v_cvt_pk_f16_f32 v39, v44, v45
	v_cvt_pk_f16_f32 v40, v46, v47
	v_cvt_pk_f16_f32 v41, v48, v49
	v_cvt_pk_f16_f32 v50, v50, v51
	v_cvt_pk_f16_f32 v51, v52, v53
	v_cvt_pk_f16_f32 v52, v54, v55
	v_cvt_pk_f16_f32 v53, v56, v57
	v_cvt_pk_f16_f32 v54, v58, v59
	v_cvt_pk_f16_f32 v55, v60, v61
	v_cvt_pk_f16_f32 v56, v62, v63
	v_cvt_pk_f16_f32 v57, v64, v65
	v_mfma_f32_32x32x16_f16 v[190:205], v[34:37], v[118:121], 0
	v_cvt_pk_f16_f32 v2, v2, v3
	v_cvt_pk_f16_f32 v3, v4, v5
	v_cvt_pk_f16_f32 v4, v6, v7
	v_cvt_pk_f16_f32 v5, v8, v9
	v_mfma_f32_32x32x16_f16 v[206:221], v[34:37], v[102:105], 0
	v_cvt_pk_f16_f32 v6, v10, v11
	v_cvt_pk_f16_f32 v7, v12, v13
	v_cvt_pk_f16_f32 v8, v14, v15
	v_cvt_pk_f16_f32 v9, v16, v17
	v_cvt_pk_f16_f32 v18, v18, v19
	v_mfma_f32_32x32x16_f16 v[190:205], v[38:41], v[114:117], v[190:205]
	v_cvt_pk_f16_f32 v19, v20, v21
	v_cvt_pk_f16_f32 v20, v22, v23
	v_cvt_pk_f16_f32 v21, v24, v25
	v_cvt_pk_f16_f32 v22, v26, v27
	v_mfma_f32_32x32x16_f16 v[206:221], v[38:41], v[98:101], v[206:221]
	v_cvt_pk_f16_f32 v23, v28, v29
	v_cvt_pk_f16_f32 v24, v30, v31
	v_cvt_pk_f16_f32 v25, v32, v33
	s_waitcnt lgkmcnt(0)
	v_mul_f32_e32 v66, v231, v239
	v_mfma_f32_32x32x16_f16 v[190:205], v[50:53], v[110:113], v[190:205]
	v_mul_f32_e32 v68, v231, v238
	v_mul_f32_e32 v67, v231, v241
	v_mul_f32_e32 v69, v231, v240
	v_fma_f32 v66, v230, v238, -v66
	v_fma_f32 v68, v230, v239, v68
	v_mfma_f32_32x32x16_f16 v[206:221], v[50:53], v[94:97], v[206:221]
	v_fma_f32 v67, v230, v240, -v67
	v_fma_f32 v69, v230, v241, v69
	v_cvt_pk_f16_f32 v246, v66, v67
	v_cvt_pk_f16_f32 v248, v68, v69
	v_mfma_f32_32x32x16_f16 v[190:205], v[54:57], v[106:109], v[190:205]
	v_mul_f32_e32 v70, v233, v243
	v_mul_f32_e32 v72, v233, v242
	v_mul_f32_e32 v71, v233, v245
	v_mul_f32_e32 v73, v233, v244
	v_fma_f32 v70, v232, v242, -v70
	v_mfma_f32_32x32x16_f16 v[206:221], v[54:57], v[90:93], v[206:221]
	v_fma_f32 v72, v232, v243, v72
	v_fma_f32 v71, v232, v244, -v71
	v_fma_f32 v73, v232, v245, v73
	v_cvt_pk_f16_f32 v247, v70, v71
	v_cvt_pk_f16_f32 v249, v72, v73
	v_mfma_f32_32x32x16_f16 v[34:49], v[2:5], v[150:153], 0
	v_mul_f32_e32 v66, v235, v239
	v_mul_f32_e32 v68, v235, v238
	v_mul_f32_e32 v67, v235, v241
	v_mul_f32_e32 v69, v235, v240
	v_fma_f32 v66, v234, v238, -v66
	v_mfma_f32_32x32x16_f16 v[34:49], v[18:21], v[146:149], v[34:49]
	v_fma_f32 v68, v234, v239, v68
	v_fma_f32 v67, v234, v240, -v67
	v_fma_f32 v69, v234, v241, v69
	v_cvt_pk_f16_f32 v250, v66, v67
	v_cvt_pk_f16_f32 v252, v68, v69
	v_mfma_f32_32x32x16_f16 v[34:49], v[6:9], v[142:145], v[34:49]
	v_mul_f32_e32 v70, v237, v243
	v_mul_f32_e32 v72, v237, v242
	v_mul_f32_e32 v71, v237, v245
	v_mul_f32_e32 v73, v237, v244
	v_fma_f32 v70, v236, v242, -v70
	v_mfma_f32_32x32x16_f16 v[34:49], v[22:25], v[138:141], v[34:49]
	v_fma_f32 v72, v236, v243, v72
	v_fma_f32 v71, v236, v244, -v71
	v_fma_f32 v73, v236, v245, v73
	v_cvt_pk_f16_f32 v251, v70, v71
	v_cvt_pk_f16_f32 v253, v72, v73
	v_cvt_pk_f16_f32 v190, v190, v191
	v_mfma_f32_32x32x16_f16 v[50:65], v[2:5], v[134:137], 0
	v_cvt_pk_f16_f32 v191, v192, v193
	v_cvt_pk_f16_f32 v192, v194, v195
	v_cvt_pk_f16_f32 v193, v196, v197
	v_cvt_pk_f16_f32 v194, v198, v199
	v_cvt_pk_f16_f32 v195, v200, v201
	v_mfma_f32_32x32x16_f16 v[50:65], v[18:21], v[126:129], v[50:65]
	v_cvt_pk_f16_f32 v196, v202, v203
	v_cvt_pk_f16_f32 v197, v204, v205
	v_cvt_pk_f16_f32 v206, v206, v207
	v_cvt_pk_f16_f32 v207, v208, v209
	v_cvt_pk_f16_f32 v208, v210, v211
	v_mfma_f32_32x32x16_f16 v[50:65], v[6:9], v[122:125], v[50:65]
	v_cvt_pk_f16_f32 v209, v212, v213
	v_cvt_pk_f16_f32 v210, v214, v215
	v_cvt_pk_f16_f32 v211, v216, v217
	v_cvt_pk_f16_f32 v212, v218, v219
	v_cvt_pk_f16_f32 v213, v220, v221
	v_mfma_f32_32x32x16_f16 v[50:65], v[22:25], v[130:133], v[50:65]
	v_xor_b32_e32 v74, 0x8a0, v173
	v_xor_b32_e32 v75, 0x8a0, v172
	ds_write_b128 v74, v[190:193]
	ds_write_b128 v75, v[194:197]
	ds_write_b128 v74, v[206:209] offset:32768
	ds_write_b128 v75, v[210:213] offset:32768
	s_nop 0
	v_mfma_f32_32x32x16_f16 v[2:17], v[222:225], v[246:249], 0
	v_mfma_f32_32x32x16_f16 v[18:33], v[226:229], v[250:253], 0
	v_cvt_pk_f16_f32 v34, v34, v35
	v_cvt_pk_f16_f32 v35, v36, v37
	v_cvt_pk_f16_f32 v36, v38, v39
	v_cvt_pk_f16_f32 v37, v40, v41
	v_cvt_pk_f16_f32 v38, v42, v43
	v_cvt_pk_f16_f32 v39, v44, v45
	v_cvt_pk_f16_f32 v40, v46, v47
	v_cvt_pk_f16_f32 v41, v48, v49
	v_cvt_pk_f16_f32 v50, v50, v51
	v_cvt_pk_f16_f32 v51, v52, v53
	v_cvt_pk_f16_f32 v52, v54, v55
	v_cvt_pk_f16_f32 v53, v56, v57
	v_cvt_pk_f16_f32 v54, v58, v59
	v_cvt_pk_f16_f32 v55, v60, v61
	v_cvt_pk_f16_f32 v56, v62, v63
	v_cvt_pk_f16_f32 v57, v64, v65
	v_mfma_f32_32x32x16_f16 v[190:205], v[34:37], v[118:121], 0
	v_cvt_pk_f16_f32 v2, v2, v3
	v_cvt_pk_f16_f32 v3, v4, v5
	v_mfma_f32_32x32x16_f16 v[206:221], v[34:37], v[102:105], 0
	v_cvt_pk_f16_f32 v4, v6, v7
	v_cvt_pk_f16_f32 v5, v8, v9
	v_mfma_f32_32x32x16_f16 v[190:205], v[38:41], v[114:117], v[190:205]
	v_cvt_pk_f16_f32 v6, v10, v11
	v_cvt_pk_f16_f32 v7, v12, v13
	v_mfma_f32_32x32x16_f16 v[206:221], v[38:41], v[98:101], v[206:221]
	v_cvt_pk_f16_f32 v8, v14, v15
	v_cvt_pk_f16_f32 v9, v16, v17
	v_mfma_f32_32x32x16_f16 v[190:205], v[50:53], v[110:113], v[190:205]
	v_cvt_pk_f16_f32 v18, v18, v19
	v_cvt_pk_f16_f32 v19, v20, v21
	v_mfma_f32_32x32x16_f16 v[206:221], v[50:53], v[94:97], v[206:221]
	v_cvt_pk_f16_f32 v20, v22, v23
	v_cvt_pk_f16_f32 v21, v24, v25
	v_mfma_f32_32x32x16_f16 v[190:205], v[54:57], v[106:109], v[190:205]
	v_cvt_pk_f16_f32 v22, v26, v27
	v_cvt_pk_f16_f32 v23, v28, v29
	v_mfma_f32_32x32x16_f16 v[206:221], v[54:57], v[90:93], v[206:221]
	v_cvt_pk_f16_f32 v24, v30, v31
	v_cvt_pk_f16_f32 v25, v32, v33
	v_mfma_f32_32x32x16_f16 v[34:49], v[2:5], v[150:153], 0
	v_mfma_f32_32x32x16_f16 v[34:49], v[18:21], v[146:149], v[34:49]
	v_mfma_f32_32x32x16_f16 v[34:49], v[6:9], v[142:145], v[34:49]
	v_mfma_f32_32x32x16_f16 v[34:49], v[22:25], v[138:141], v[34:49]
	v_mfma_f32_32x32x16_f16 v[50:65], v[2:5], v[134:137], 0
	s_nop 5
	v_cvt_pk_f16_f32 v190, v190, v191
	v_cvt_pk_f16_f32 v191, v192, v193
	v_cvt_pk_f16_f32 v192, v194, v195
	v_cvt_pk_f16_f32 v193, v196, v197
	v_mfma_f32_32x32x16_f16 v[50:65], v[18:21], v[126:129], v[50:65]
	v_cvt_pk_f16_f32 v194, v198, v199
	v_cvt_pk_f16_f32 v195, v200, v201
	v_cvt_pk_f16_f32 v196, v202, v203
	v_cvt_pk_f16_f32 v197, v204, v205
	v_cvt_pk_f16_f32 v206, v206, v207
	v_cvt_pk_f16_f32 v207, v208, v209
	v_mfma_f32_32x32x16_f16 v[50:65], v[6:9], v[122:125], v[50:65]
	v_cvt_pk_f16_f32 v208, v210, v211
	v_cvt_pk_f16_f32 v209, v212, v213
	v_cvt_pk_f16_f32 v210, v214, v215
	v_cvt_pk_f16_f32 v211, v216, v217
	v_cvt_pk_f16_f32 v212, v218, v219
	v_cvt_pk_f16_f32 v213, v220, v221
	v_mfma_f32_32x32x16_f16 v[50:65], v[22:25], v[130:133], v[50:65]
	v_xor_b32_e32 v74, 0x1040, v173
	v_xor_b32_e32 v75, 0x1040, v172
	ds_write_b128 v74, v[190:193]
	ds_write_b128 v75, v[194:197]
	ds_write_b128 v74, v[206:209] offset:32768
	ds_write_b128 v75, v[210:213] offset:32768
	s_nop 11
	v_cvt_pk_f16_f32 v34, v34, v35
	v_cvt_pk_f16_f32 v35, v36, v37
	v_cvt_pk_f16_f32 v36, v38, v39
	v_cvt_pk_f16_f32 v37, v40, v41
	v_cvt_pk_f16_f32 v38, v42, v43
	v_cvt_pk_f16_f32 v39, v44, v45
	v_cvt_pk_f16_f32 v40, v46, v47
	v_cvt_pk_f16_f32 v41, v48, v49
	v_cvt_pk_f16_f32 v50, v50, v51
	v_cvt_pk_f16_f32 v51, v52, v53
	v_cvt_pk_f16_f32 v52, v54, v55
	v_cvt_pk_f16_f32 v53, v56, v57
	v_cvt_pk_f16_f32 v54, v58, v59
	v_cvt_pk_f16_f32 v55, v60, v61
	v_cvt_pk_f16_f32 v56, v62, v63
	v_cvt_pk_f16_f32 v57, v64, v65
	v_mfma_f32_32x32x16_f16 v[190:205], v[34:37], v[118:121], 0
	v_mfma_f32_32x32x16_f16 v[206:221], v[34:37], v[102:105], 0
	v_mfma_f32_32x32x16_f16 v[190:205], v[38:41], v[114:117], v[190:205]
	v_mfma_f32_32x32x16_f16 v[206:221], v[38:41], v[98:101], v[206:221]
	v_mfma_f32_32x32x16_f16 v[190:205], v[50:53], v[110:113], v[190:205]
	v_mfma_f32_32x32x16_f16 v[206:221], v[50:53], v[94:97], v[206:221]
	v_mfma_f32_32x32x16_f16 v[190:205], v[54:57], v[106:109], v[190:205]
	v_mfma_f32_32x32x16_f16 v[206:221], v[54:57], v[90:93], v[206:221]
	v_and_b32_e32 v134, 1, v156
	v_bitop3_b32 v132, v171, s40, v170 bitop3:0x36
	v_bitop3_b32 v131, s41, v154, v160 bitop3:0x36
	v_bitop3_b32 v135, v171, s42, v170 bitop3:0x36
	v_xor_b32_e32 v133, s43, v154
	v_and_b32_e32 v130, 4, v156
	s_lshl_b32 s2, s27, 3
	s_lshl_b32 s3, s5, 2
	s_or_b32 s2, s3, s2
	s_ashr_i32 s3, s2, 31
	s_lshl_b64 s[2:3], s[2:3], 13
	s_add_u32 s2, s20, s2
	s_addc_u32 s3, s21, s3
	v_lshlrev_b32_e32 v154, 1, v169
	v_lshl_add_u64 v[2:3], s[2:3], 0, v[154:155]
	v_add_co_u32_e32 v2, vcc, s23, v2
	s_nop 1
	v_addc_co_u32_e32 v3, vcc, 0, v3, vcc
	v_cvt_pk_f16_f32 v190, v190, v191
	v_cvt_pk_f16_f32 v191, v192, v193
	v_cvt_pk_f16_f32 v192, v194, v195
	v_cvt_pk_f16_f32 v193, v196, v197
	v_cvt_pk_f16_f32 v194, v198, v199
	v_cvt_pk_f16_f32 v195, v200, v201
	v_cvt_pk_f16_f32 v196, v202, v203
	v_cvt_pk_f16_f32 v197, v204, v205
	v_cvt_pk_f16_f32 v206, v206, v207
	v_cvt_pk_f16_f32 v207, v208, v209
	v_cvt_pk_f16_f32 v208, v210, v211
	v_cvt_pk_f16_f32 v209, v212, v213
	v_cvt_pk_f16_f32 v210, v214, v215
	v_cvt_pk_f16_f32 v211, v216, v217
	v_cvt_pk_f16_f32 v212, v218, v219
	v_cvt_pk_f16_f32 v213, v220, v221
	v_xor_b32_e32 v74, 0x18e0, v173
	v_xor_b32_e32 v75, 0x18e0, v172
	ds_write_b128 v74, v[190:193]
	ds_write_b128 v75, v[194:197]
	ds_write_b128 v74, v[206:209] offset:32768
	ds_write_b128 v75, v[210:213] offset:32768
	s_setprio 0
	s_waitcnt lgkmcnt(0)
	s_barrier
	global_load_dwordx4 v[62:65], v154, s[2:3]
	global_load_dwordx4 v[46:49], v154, s[2:3] offset:1024
	global_load_dwordx4 v[42:45], v154, s[2:3] offset:2048
	global_load_dwordx4 v[38:41], v154, s[2:3] offset:3072
	global_load_dwordx4 v[54:57], v[2:3], off offset:1024
	global_load_dwordx4 v[50:53], v[2:3], off offset:2048
	v_lshl_add_u64 v[4:5], s[12:13], 0, v[154:155]
	global_load_dwordx4 v[126:129], v154, s[12:13]
	global_load_dwordx4 v[122:125], v154, s[12:13] offset:1024
	global_load_dwordx4 v[118:121], v154, s[12:13] offset:2048
	global_load_dwordx4 v[114:117], v154, s[12:13] offset:3072
	global_load_dwordx4 v[34:37], v168, s[2:3]
	global_load_dwordx4 v[110:113], v168, s[12:13]
	v_add_co_u32_e32 v4, vcc, s23, v4
	s_nop 1
	v_addc_co_u32_e32 v5, vcc, 0, v5, vcc
	global_load_dwordx4 v[58:61], v[2:3], off offset:3072
	global_load_dwordx4 v[106:109], v[4:5], off offset:1024
	global_load_dwordx4 v[94:97], v[4:5], off offset:2048
	global_load_dwordx4 v[90:93], v[4:5], off offset:3072
	v_bfrev_b32_e32 v3, v156
	v_lshlrev_b32_e32 v7, 5, v167
	v_lshlrev_b32_e32 v6, 9, v167
	v_and_b32_e32 v7, 0x200, v7
	v_lshlrev_b32_e32 v8, 8, v167
	v_lshrrev_b32_e32 v3, 27, v3
	v_lshrrev_b32_e32 v2, 2, v167
	v_lshrrev_b32_e32 v4, 4, v156
	v_xor_b32_e32 v5, v169, v156
	v_and_b32_e32 v6, 0x5800, v6
	v_and_b32_e32 v3, 8, v3
	v_and_or_b32 v7, v8, s24, v7
	v_lshrrev_b32_e32 v5, 1, v5
	v_xor_b32_e32 v4, v2, v4
	v_or3_b32 v3, v7, v6, v3
	v_bitop3_b32 v7, v2, v182, 1 bitop3:0x6c
	v_lshlrev_b32_e32 v2, 1, v167
	v_and_b32_e32 v5, 4, v5
	v_lshlrev_b32_e32 v4, 3, v4
	v_lshrrev_b32_e32 v6, 1, v167
	v_and_b32_e32 v2, 2, v2
	v_and_or_b32 v9, v169, 8, v2
	v_and_b32_e32 v2, 8, v4
	v_and_or_b32 v4, v6, 2, v5
	v_or3_b32 v2, v4, v2, v134
	v_lshlrev_b32_e32 v2, 4, v2
	v_bitop3_b32 v146, v3, s28, v2 bitop3:0x36
	v_xor_b32_e32 v8, v6, v182
	v_xor_b32_e32 v147, 0x2010, v146
	ds_read_b64_tr_b16 v[2:3], v146
	ds_read_b64_tr_b16 v[4:5], v147
	v_lshlrev_b32_e32 v8, 2, v8
	v_and_b32_e32 v8, 4, v8
	v_or3_b32 v6, v9, v7, v8
	v_lshlrev_b32_e32 v7, 11, v167
	v_and_b32_e32 v8, 0x7800, v7
	v_lshlrev_b32_e32 v6, 4, v6
	v_or3_b32 v22, v6, v8, v170
	v_and_b32_e32 v23, 0x8000, v7
	s_waitcnt vmcnt(17) lgkmcnt(0)
	v_mfma_f32_32x32x16_f16 v[2:17], v[2:5], v[86:89], 0
	ds_read_b64_tr_b16 v[20:21], v147 offset:32768
	ds_read_b64_tr_b16 v[18:19], v146 offset:32768
	v_xor_b32_e32 v150, 16, v146
	v_xad_u32 v70, v22, s28, v23
	v_xor_b32_e32 v151, 0x2000, v146
	ds_read_b64_tr_b16 v[22:23], v150
	ds_read_b64_tr_b16 v[24:25], v151
	ds_read_b64_tr_b16 v[28:29], v151 offset:32768
	ds_read_b64_tr_b16 v[26:27], v150 offset:32768
	v_xor_b32_e32 v30, 0x280, v70
	v_xor_b32_e32 v148, 32, v146
	s_waitcnt vmcnt(16) lgkmcnt(4)
	v_mfma_f32_32x32x16_f16 v[2:17], v[18:21], v[82:85], v[2:17]
	v_xor_b32_e32 v149, 0x2030, v146
	v_xor_b32_e32 v144, 48, v146
	v_xor_b32_e32 v145, 0x2020, v146
	v_xor_b32_e32 v142, 64, v146
	v_xor_b32_e32 v143, 0x2050, v146
	v_xor_b32_e32 v140, 0x50, v146
	v_xor_b32_e32 v141, 0x2040, v146
	s_nop 4
	v_cvt_pk_f16_f32 v9, v8, v9
	v_cvt_pk_f16_f32 v8, v6, v7
	v_cvt_pk_f16_f32 v7, v4, v5
	v_cvt_pk_f16_f32 v6, v2, v3
	ds_write_b128 v70, v[6:9]
	v_cvt_pk_f16_f32 v21, v16, v17
	v_cvt_pk_f16_f32 v20, v14, v15
	v_cvt_pk_f16_f32 v19, v12, v13
	v_cvt_pk_f16_f32 v18, v10, v11
	s_waitcnt lgkmcnt(3)
	v_mfma_f32_32x32x16_f16 v[2:17], v[22:25], v[86:89], 0
	ds_write_b128 v30, v[18:21]
	ds_read_b64_tr_b16 v[18:19], v148
	ds_read_b64_tr_b16 v[20:21], v149
	ds_read_b64_tr_b16 v[24:25], v149 offset:32768
	ds_read_b64_tr_b16 v[22:23], v148 offset:32768
	v_xor_b32_e32 v30, 0x290, v70
	v_xor_b32_e32 v138, 0x60, v146
	v_xor_b32_e32 v139, 0x2070, v146
	v_xor_b32_e32 v136, 0x70, v146
	v_xor_b32_e32 v137, 0x2060, v146
	s_waitcnt lgkmcnt(6)
	v_mfma_f32_32x32x16_f16 v[2:17], v[26:29], v[82:85], v[2:17]
	v_xor_b32_e32 v26, 16, v70
	v_xor_b32_e32 v71, 0x60, v70
	s_lshl_b64 s[0:1], s[0:1], 13
	s_add_u32 s0, s8, s0
	s_addc_u32 s1, s9, s1
	s_nop 6
	v_cvt_pk_f16_f32 v9, v8, v9
	v_cvt_pk_f16_f32 v8, v6, v7
	v_cvt_pk_f16_f32 v7, v4, v5
	v_cvt_pk_f16_f32 v6, v2, v3
	ds_write_b128 v26, v[6:9]
	v_cvt_pk_f16_f32 v29, v16, v17
	v_cvt_pk_f16_f32 v28, v14, v15
	v_cvt_pk_f16_f32 v27, v12, v13
	v_cvt_pk_f16_f32 v26, v10, v11
	s_waitcnt lgkmcnt(3)
	v_mfma_f32_32x32x16_f16 v[2:17], v[18:21], v[86:89], 0
	ds_write_b128 v30, v[26:29]
	ds_read_b64_tr_b16 v[18:19], v144
	ds_read_b64_tr_b16 v[20:21], v145
	ds_read_b64_tr_b16 v[28:29], v145 offset:32768
	ds_read_b64_tr_b16 v[26:27], v144 offset:32768
	v_xor_b32_e32 v30, 0x2a0, v70
	s_waitcnt lgkmcnt(6)
	v_mfma_f32_32x32x16_f16 v[2:17], v[22:25], v[82:85], v[2:17]
	v_xor_b32_e32 v22, 32, v70
	s_nop 10
	v_cvt_pk_f16_f32 v9, v8, v9
	v_cvt_pk_f16_f32 v8, v6, v7
	v_cvt_pk_f16_f32 v7, v4, v5
	v_cvt_pk_f16_f32 v6, v2, v3
	ds_write_b128 v22, v[6:9]
	v_cvt_pk_f16_f32 v25, v16, v17
	v_cvt_pk_f16_f32 v24, v14, v15
	v_cvt_pk_f16_f32 v23, v12, v13
	v_cvt_pk_f16_f32 v22, v10, v11
	s_waitcnt lgkmcnt(3)
	v_mfma_f32_32x32x16_f16 v[2:17], v[18:21], v[86:89], 0
	ds_write_b128 v30, v[22:25]
	ds_read_b64_tr_b16 v[18:19], v142
	ds_read_b64_tr_b16 v[20:21], v143
	ds_read_b64_tr_b16 v[24:25], v143 offset:32768
	ds_read_b64_tr_b16 v[22:23], v142 offset:32768
	v_xor_b32_e32 v30, 0x2b0, v70
	s_waitcnt lgkmcnt(6)
	v_mfma_f32_32x32x16_f16 v[2:17], v[26:29], v[82:85], v[2:17]
	v_xor_b32_e32 v26, 48, v70
	s_nop 10
	v_cvt_pk_f16_f32 v9, v8, v9
	v_cvt_pk_f16_f32 v8, v6, v7
	v_cvt_pk_f16_f32 v7, v4, v5
	v_cvt_pk_f16_f32 v6, v2, v3
	ds_write_b128 v26, v[6:9]
	v_cvt_pk_f16_f32 v29, v16, v17
	v_cvt_pk_f16_f32 v28, v14, v15
	v_cvt_pk_f16_f32 v27, v12, v13
	v_cvt_pk_f16_f32 v26, v10, v11
	s_waitcnt lgkmcnt(3)
	v_mfma_f32_32x32x16_f16 v[2:17], v[18:21], v[86:89], 0
	ds_write_b128 v30, v[26:29]
	ds_read_b64_tr_b16 v[18:19], v140
	ds_read_b64_tr_b16 v[20:21], v141
	ds_read_b64_tr_b16 v[28:29], v141 offset:32768
	ds_read_b64_tr_b16 v[26:27], v140 offset:32768
	s_waitcnt lgkmcnt(6)
	v_mfma_f32_32x32x16_f16 v[2:17], v[22:25], v[82:85], v[2:17]
	v_xor_b32_e32 v22, 64, v70
	s_nop 10
	v_cvt_pk_f16_f32 v9, v8, v9
	v_cvt_pk_f16_f32 v8, v6, v7
	v_cvt_pk_f16_f32 v7, v4, v5
	v_cvt_pk_f16_f32 v6, v2, v3
	ds_write_b128 v22, v[6:9]
	v_cvt_pk_f16_f32 v5, v16, v17
	v_cvt_pk_f16_f32 v4, v14, v15
	v_cvt_pk_f16_f32 v3, v12, v13
	v_cvt_pk_f16_f32 v2, v10, v11
	s_waitcnt lgkmcnt(3)
	v_mfma_f32_32x32x16_f16 v[10:25], v[18:21], v[86:89], 0
	v_xor_b32_e32 v6, 0x2c0, v70
	ds_write_b128 v6, v[2:5]
	ds_read_b64_tr_b16 v[2:3], v138
	ds_read_b64_tr_b16 v[4:5], v139
	ds_read_b64_tr_b16 v[32:33], v139 offset:32768
	ds_read_b64_tr_b16 v[30:31], v138 offset:32768
	s_waitcnt lgkmcnt(6)
	v_mfma_f32_32x32x16_f16 v[10:25], v[26:29], v[82:85], v[10:25]
	v_xor_b32_e32 v26, 0x50, v70
	s_nop 10
	v_cvt_pk_f16_f32 v9, v16, v17
	v_cvt_pk_f16_f32 v8, v14, v15
	v_cvt_pk_f16_f32 v7, v12, v13
	v_cvt_pk_f16_f32 v6, v10, v11
	ds_write_b128 v26, v[6:9]
	s_waitcnt lgkmcnt(3)
	v_mfma_f32_32x32x16_f16 v[2:17], v[2:5], v[86:89], 0
	v_cvt_pk_f16_f32 v25, v24, v25
	v_cvt_pk_f16_f32 v24, v22, v23
	v_cvt_pk_f16_f32 v23, v20, v21
	v_cvt_pk_f16_f32 v22, v18, v19
	v_xor_b32_e32 v18, 0x2d0, v70
	ds_write_b128 v18, v[22:25]
	ds_read_b64_tr_b16 v[18:19], v136
	ds_read_b64_tr_b16 v[20:21], v137
	s_waitcnt lgkmcnt(4)
	v_mfma_f32_32x32x16_f16 v[2:17], v[30:33], v[82:85], v[2:17]
	ds_read_b64_tr_b16 v[68:69], v137 offset:32768
	ds_read_b64_tr_b16 v[66:67], v136 offset:32768
	s_waitcnt lgkmcnt(2)
	v_mfma_f32_32x32x16_f16 v[18:33], v[18:21], v[86:89], 0
	s_nop 7
	v_cvt_pk_f16_f32 v9, v8, v9
	v_cvt_pk_f16_f32 v8, v6, v7
	v_cvt_pk_f16_f32 v7, v4, v5
	v_cvt_pk_f16_f32 v6, v2, v3
	ds_write_b128 v71, v[6:9]
	v_cvt_pk_f16_f32 v5, v16, v17
	v_cvt_pk_f16_f32 v4, v14, v15
	s_waitcnt lgkmcnt(1)
	v_mfma_f32_32x32x16_f16 v[18:33], v[66:69], v[82:85], v[18:33]
	v_cvt_pk_f16_f32 v3, v12, v13
	v_cvt_pk_f16_f32 v2, v10, v11
	v_xor_b32_e32 v6, 0x2e0, v70
	ds_write_b128 v6, v[2:5]
	v_xor_b32_e32 v6, 0x70, v70
	s_nop 6
	v_cvt_pk_f16_f32 v5, v24, v25
	v_cvt_pk_f16_f32 v4, v22, v23
	v_cvt_pk_f16_f32 v3, v20, v21
	v_cvt_pk_f16_f32 v2, v18, v19
	ds_write_b128 v6, v[2:5]
	v_cvt_pk_f16_f32 v5, v32, v33
	v_cvt_pk_f16_f32 v4, v30, v31
	v_cvt_pk_f16_f32 v3, v28, v29
	v_cvt_pk_f16_f32 v2, v26, v27
	v_xor_b32_e32 v6, 0x2f0, v70
	ds_write_b128 v6, v[2:5]
	v_lshl_add_u64 v[2:3], s[0:1], 0, v[154:155]
	v_lshl_add_u64 v[4:5], v[2:3], 0, s[18:19]
	v_add_co_u32_e32 v2, vcc, s25, v2
	s_waitcnt lgkmcnt(0)
	s_nop 0
	v_addc_co_u32_e32 v3, vcc, 0, v3, vcc
	s_barrier
	global_load_dwordx4 v[102:105], v[2:3], off
	global_load_dwordx4 v[98:101], v[4:5], off offset:1024
	s_setprio 1
	s_add_u32 s0, s2, 0x2000
	s_addc_u32 s1, s3, 0
	v_lshl_add_u64 v[2:3], s[0:1], 0, v[154:155]
	v_add_co_u32_e32 v2, vcc, s23, v2
	global_load_dwordx4 v[66:69], v154, s[0:1]
	global_load_dwordx4 v[70:73], v154, s[0:1] offset:1024
	global_load_dwordx4 v[74:77], v154, s[0:1] offset:2048
	global_load_dwordx4 v[78:81], v154, s[0:1] offset:3072
	v_addc_co_u32_e32 v3, vcc, 0, v3, vcc
	global_load_dwordx4 v[82:85], v168, s[0:1]
	global_load_dwordx4 v[86:89], v[2:3], off offset:1024
	global_load_dwordx4 v[182:185], v[2:3], off offset:2048
	global_load_dwordx4 v[186:189], v[2:3], off offset:3072
	ds_read_b128 v[18:21], v179
	ds_read_b128 v[22:25], v179 offset:32768
	ds_read_b128 v[26:29], v178
	ds_read_b128 v[30:33], v178 offset:32768
	s_add_u32 s0, s2, 0x6000
	s_addc_u32 s1, s3, 0
	s_waitcnt vmcnt(25) lgkmcnt(3)
	v_mfma_f32_32x32x16_f16 v[2:17], v[18:21], v[62:65], 0
	s_add_u32 s2, s2, 0x4000
	s_addc_u32 s3, s3, 0
	s_or_b32 s27, s26, 0x8a0
	s_or_b32 s26, s26, 0xa20
	s_waitcnt vmcnt(24) lgkmcnt(1)
	v_mfma_f32_32x32x16_f16 v[2:17], v[26:29], v[46:49], v[2:17]
	s_waitcnt vmcnt(23)
	v_mfma_f32_32x32x16_f16 v[2:17], v[22:25], v[42:45], v[2:17]
	s_waitcnt vmcnt(22) lgkmcnt(0)
	v_mfma_f32_32x32x16_f16 v[2:17], v[30:33], v[38:41], v[2:17]
	s_waitcnt vmcnt(15)
	v_mfma_f32_32x32x16_f16 v[34:49], v[18:21], v[34:37], 0
	s_nop 9
	v_cvt_pk_f16_f32 v9, v8, v9
	v_cvt_pk_f16_f32 v8, v6, v7
	v_cvt_pk_f16_f32 v7, v4, v5
	v_cvt_pk_f16_f32 v6, v2, v3
	v_cvt_pk_f16_f32 v5, v16, v17
	v_cvt_pk_f16_f32 v4, v14, v15
	v_cvt_pk_f16_f32 v3, v12, v13
	v_mfma_f32_32x32x16_f16 v[34:49], v[26:29], v[54:57], v[34:49]
	v_cvt_pk_f16_f32 v2, v10, v11
	v_mfma_f32_32x32x16_f16 v[34:49], v[22:25], v[50:53], v[34:49]
	s_waitcnt vmcnt(13)
	v_mfma_f32_32x32x16_f16 v[34:49], v[30:33], v[58:61], v[34:49]
	v_mfma_f32_32x32x16_f16 v[18:33], v[6:9], v[126:129], 0
	s_nop 10
	v_cvt_pk_f16_f32 v13, v40, v41
	v_cvt_pk_f16_f32 v12, v38, v39
	v_cvt_pk_f16_f32 v11, v36, v37
	v_cvt_pk_f16_f32 v10, v34, v35
	v_cvt_pk_f16_f32 v17, v48, v49
	v_cvt_pk_f16_f32 v16, v46, v47
	v_cvt_pk_f16_f32 v15, v44, v45
	v_mfma_f32_32x32x16_f16 v[50:65], v[6:9], v[110:113], 0
	v_bitop3_b32 v6, v171, s27, v170 bitop3:0x36
	v_cvt_pk_f16_f32 v14, v42, v43
	v_mfma_f32_32x32x16_f16 v[18:33], v[2:5], v[122:125], v[18:33]
	s_waitcnt vmcnt(12)
	v_mfma_f32_32x32x16_f16 v[50:65], v[2:5], v[106:109], v[50:65]
	ds_read_b128 v[2:5], v6
	ds_read_b128 v[6:9], v6 offset:32768
	v_mfma_f32_32x32x16_f16 v[18:33], v[10:13], v[118:121], v[18:33]
	s_waitcnt vmcnt(11)
	v_mfma_f32_32x32x16_f16 v[50:65], v[10:13], v[94:97], v[50:65]
	s_waitcnt vmcnt(7) lgkmcnt(1)
	v_mfma_f32_32x32x16_f16 v[34:49], v[2:5], v[66:69], 0
	v_mfma_f32_32x32x16_f16 v[18:33], v[14:17], v[114:117], v[18:33]
	v_mfma_f32_32x32x16_f16 v[50:65], v[14:17], v[90:93], v[50:65]
	v_bitop3_b32 v14, v171, s26, v170 bitop3:0x36
	ds_read_b128 v[10:13], v14
	ds_read_b128 v[14:17], v14 offset:32768
	s_nop 7
	v_cvt_pk_f16_f32 v25, v24, v25
	v_cvt_pk_f16_f32 v24, v22, v23
	v_cvt_pk_f16_f32 v23, v20, v21
	v_cvt_pk_f16_f32 v22, v18, v19
	v_cvt_pk_f16_f32 v21, v32, v33
	s_waitcnt vmcnt(6) lgkmcnt(1)
	v_mfma_f32_32x32x16_f16 v[34:49], v[10:13], v[70:73], v[34:49]
	v_cvt_pk_f16_f32 v20, v30, v31
	v_cvt_pk_f16_f32 v19, v28, v29
	v_cvt_pk_f16_f32 v18, v26, v27
	ds_write_b128 v173, v[22:25]
	ds_write_b128 v172, v[18:21]
	v_cvt_pk_f16_f32 v21, v56, v57
	v_cvt_pk_f16_f32 v20, v54, v55
	s_waitcnt vmcnt(5)
	v_mfma_f32_32x32x16_f16 v[34:49], v[6:9], v[74:77], v[34:49]
	v_cvt_pk_f16_f32 v19, v52, v53
	v_cvt_pk_f16_f32 v18, v50, v51
	ds_write_b128 v173, v[18:21] offset:32768
	v_cvt_pk_f16_f32 v21, v64, v65
	v_cvt_pk_f16_f32 v20, v62, v63
	v_cvt_pk_f16_f32 v19, v60, v61
	v_cvt_pk_f16_f32 v18, v58, v59
	s_waitcnt vmcnt(4) lgkmcnt(3)
	v_mfma_f32_32x32x16_f16 v[34:49], v[14:17], v[78:81], v[34:49]
	ds_write_b128 v172, v[18:21] offset:32768
	s_waitcnt vmcnt(3)
	v_mfma_f32_32x32x16_f16 v[66:81], v[2:5], v[82:85], 0
	s_nop 8
	v_cvt_pk_f16_f32 v41, v40, v41
	v_cvt_pk_f16_f32 v40, v38, v39
	v_cvt_pk_f16_f32 v39, v36, v37
	v_cvt_pk_f16_f32 v38, v34, v35
	v_cvt_pk_f16_f32 v85, v48, v49
	v_cvt_pk_f16_f32 v84, v46, v47
	v_cvt_pk_f16_f32 v83, v44, v45
	s_waitcnt vmcnt(2)
	v_mfma_f32_32x32x16_f16 v[66:81], v[10:13], v[86:89], v[66:81]
	v_cvt_pk_f16_f32 v82, v42, v43
	s_waitcnt vmcnt(1)
	v_mfma_f32_32x32x16_f16 v[66:81], v[6:9], v[182:185], v[66:81]
	s_waitcnt vmcnt(0)
	v_mfma_f32_32x32x16_f16 v[66:81], v[14:17], v[186:189], v[66:81]
	v_mfma_f32_32x32x16_f16 v[2:17], v[38:41], v[126:129], 0
	s_nop 10
	v_cvt_pk_f16_f32 v73, v72, v73
	v_cvt_pk_f16_f32 v72, v70, v71
	v_cvt_pk_f16_f32 v70, v66, v67
	v_cvt_pk_f16_f32 v67, v76, v77
	v_cvt_pk_f16_f32 v66, v74, v75
	global_load_dwordx4 v[74:77], v154, s[2:3]
	v_cvt_pk_f16_f32 v71, v68, v69
	v_cvt_pk_f16_f32 v69, v80, v81
	v_cvt_pk_f16_f32 v68, v78, v79
	global_load_dwordx4 v[78:81], v154, s[2:3] offset:1024
	ds_read_b128 v[18:21], v180
	ds_read_b128 v[22:25], v176
	ds_read_b128 v[26:29], v180 offset:32768
	global_load_dwordx4 v[30:33], v154, s[2:3] offset:2048
	v_mfma_f32_32x32x16_f16 v[34:49], v[38:41], v[110:113], 0
	v_mfma_f32_32x32x16_f16 v[2:17], v[82:85], v[122:125], v[2:17]
	v_mfma_f32_32x32x16_f16 v[34:49], v[82:85], v[106:109], v[34:49]
	ds_read_b128 v[82:85], v176 offset:32768
	s_waitcnt vmcnt(2) lgkmcnt(3)
	v_mfma_f32_32x32x16_f16 v[50:65], v[18:21], v[74:77], 0
	v_mfma_f32_32x32x16_f16 v[2:17], v[70:73], v[118:121], v[2:17]
	v_mfma_f32_32x32x16_f16 v[34:49], v[70:73], v[94:97], v[34:49]
	v_lshl_add_u64 v[70:71], s[2:3], 0, v[154:155]
	v_add_co_u32_e32 v152, vcc, s23, v70
	s_nop 1
	v_addc_co_u32_e32 v153, vcc, 0, v71, vcc
	s_waitcnt vmcnt(1) lgkmcnt(2)
	v_mfma_f32_32x32x16_f16 v[50:65], v[22:25], v[78:81], v[50:65]
	v_mfma_f32_32x32x16_f16 v[2:17], v[66:69], v[114:117], v[2:17]
	v_mfma_f32_32x32x16_f16 v[34:49], v[66:69], v[90:93], v[34:49]
	global_load_dwordx4 v[66:69], v154, s[2:3] offset:3072
	s_nop 9
	v_cvt_pk_f16_f32 v9, v8, v9
	v_cvt_pk_f16_f32 v8, v6, v7
	v_cvt_pk_f16_f32 v7, v4, v5
	v_cvt_pk_f16_f32 v6, v2, v3
	v_cvt_pk_f16_f32 v5, v16, v17
	v_cvt_pk_f16_f32 v4, v14, v15
	s_waitcnt vmcnt(1) lgkmcnt(1)
	v_mfma_f32_32x32x16_f16 v[50:65], v[26:29], v[30:33], v[50:65]
	global_load_dwordx4 v[30:33], v168, s[2:3]
	global_load_dwordx4 v[86:89], v[152:153], off offset:1024
	s_nop 0
	global_load_dwordx4 v[168:171], v168, s[0:1]
	v_cvt_pk_f16_f32 v3, v12, v13
	v_cvt_pk_f16_f32 v2, v10, v11
	ds_write_b128 v175, v[6:9]
	ds_write_b128 v174, v[2:5]
	v_cvt_pk_f16_f32 v5, v40, v41
	s_waitcnt vmcnt(3) lgkmcnt(2)
	v_mfma_f32_32x32x16_f16 v[50:65], v[82:85], v[66:69], v[50:65]
	global_load_dwordx4 v[182:185], v154, s[0:1] offset:1024
	v_cvt_pk_f16_f32 v4, v38, v39
	v_cvt_pk_f16_f32 v3, v36, v37
	v_cvt_pk_f16_f32 v2, v34, v35
	ds_write_b128 v175, v[2:5] offset:32768
	v_cvt_pk_f16_f32 v5, v48, v49
	v_cvt_pk_f16_f32 v4, v46, v47
	s_waitcnt vmcnt(3)
	v_mfma_f32_32x32x16_f16 v[66:81], v[18:21], v[30:33], 0
	global_load_dwordx4 v[18:21], v[152:153], off offset:2048
	v_cvt_pk_f16_f32 v3, v44, v45
	v_cvt_pk_f16_f32 v2, v42, v43
	ds_write_b128 v174, v[2:5] offset:32768
	v_cvt_pk_f16_f32 v57, v56, v57
	v_cvt_pk_f16_f32 v56, v54, v55
	v_cvt_pk_f16_f32 v55, v52, v53
	s_waitcnt vmcnt(3)
	v_mfma_f32_32x32x16_f16 v[66:81], v[22:25], v[86:89], v[66:81]
	global_load_dwordx4 v[22:25], v[152:153], off offset:3072
	v_cvt_pk_f16_f32 v54, v50, v51
	s_waitcnt vmcnt(1)
	v_mfma_f32_32x32x16_f16 v[66:81], v[26:29], v[18:21], v[66:81]
	v_lshl_add_u64 v[18:19], s[0:1], 0, v[154:155]
	v_add_co_u32_e32 v152, vcc, s23, v18
	s_nop 1
	v_addc_co_u32_e32 v153, vcc, 0, v19, vcc
	global_load_dwordx4 v[86:89], v[152:153], off offset:1024
	s_waitcnt vmcnt(1)
	v_mfma_f32_32x32x16_f16 v[66:81], v[82:85], v[22:25], v[66:81]
	v_cvt_pk_f16_f32 v85, v64, v65
	v_cvt_pk_f16_f32 v84, v62, v63
	v_cvt_pk_f16_f32 v83, v60, v61
	v_cvt_pk_f16_f32 v82, v58, v59
	v_mfma_f32_32x32x16_f16 v[18:33], v[54:57], v[126:129], 0
	s_nop 6
	v_cvt_pk_f16_f32 v73, v72, v73
	v_cvt_pk_f16_f32 v72, v70, v71
	v_cvt_pk_f16_f32 v70, v66, v67
	v_cvt_pk_f16_f32 v67, v76, v77
	v_cvt_pk_f16_f32 v66, v74, v75
	global_load_dwordx4 v[74:77], v154, s[0:1]
	ds_read_b128 v[2:5], v181
	ds_read_b128 v[6:9], v177
	ds_read_b128 v[10:13], v181 offset:32768
	global_load_dwordx4 v[14:17], v154, s[0:1] offset:2048
	global_load_dwordx4 v[34:37], v154, s[0:1] offset:3072
	v_mfma_f32_32x32x16_f16 v[50:65], v[54:57], v[110:113], 0
	v_cvt_pk_f16_f32 v71, v68, v69
	v_cvt_pk_f16_f32 v69, v80, v81
	v_cvt_pk_f16_f32 v68, v78, v79
	v_mfma_f32_32x32x16_f16 v[18:33], v[82:85], v[122:125], v[18:33]
	v_mfma_f32_32x32x16_f16 v[50:65], v[82:85], v[106:109], v[50:65]
	ds_read_b128 v[82:85], v177 offset:32768
	v_mfma_f32_32x32x16_f16 v[18:33], v[70:73], v[118:121], v[18:33]
	v_mfma_f32_32x32x16_f16 v[50:65], v[70:73], v[94:97], v[50:65]
	v_mfma_f32_32x32x16_f16 v[18:33], v[66:69], v[114:117], v[18:33]
	v_mfma_f32_32x32x16_f16 v[50:65], v[66:69], v[90:93], v[50:65]
	s_nop 10
	v_cvt_pk_f16_f32 v25, v24, v25
	v_cvt_pk_f16_f32 v24, v22, v23
	v_cvt_pk_f16_f32 v23, v20, v21
	v_cvt_pk_f16_f32 v22, v18, v19
	ds_write_b128 v132, v[22:25]
	s_waitcnt vmcnt(2) lgkmcnt(4)
	v_mfma_f32_32x32x16_f16 v[66:81], v[2:5], v[74:77], 0
	s_waitcnt lgkmcnt(3)
	v_mfma_f32_32x32x16_f16 v[66:81], v[6:9], v[182:185], v[66:81]
	s_waitcnt vmcnt(1) lgkmcnt(2)
	v_mfma_f32_32x32x16_f16 v[66:81], v[10:13], v[14:17], v[66:81]
	s_waitcnt vmcnt(0) lgkmcnt(1)
	v_mfma_f32_32x32x16_f16 v[66:81], v[82:85], v[34:37], v[66:81]
	v_mfma_f32_32x32x16_f16 v[34:49], v[2:5], v[168:171], 0
	global_load_dwordx4 v[2:5], v[152:153], off offset:2048
	s_nop 9
	v_cvt_pk_f16_f32 v73, v72, v73
	v_cvt_pk_f16_f32 v72, v70, v71
	v_cvt_pk_f16_f32 v71, v68, v69
	v_cvt_pk_f16_f32 v70, v66, v67
	v_cvt_pk_f16_f32 v69, v80, v81
	v_cvt_pk_f16_f32 v68, v78, v79
	v_mfma_f32_32x32x16_f16 v[34:49], v[6:9], v[86:89], v[34:49]
	global_load_dwordx4 v[6:9], v[152:153], off offset:3072
	v_cvt_pk_f16_f32 v67, v76, v77
	v_cvt_pk_f16_f32 v66, v74, v75
	s_waitcnt vmcnt(1)
	v_mfma_f32_32x32x16_f16 v[34:49], v[10:13], v[2:5], v[34:49]
	s_waitcnt vmcnt(0)
	v_mfma_f32_32x32x16_f16 v[34:49], v[82:85], v[6:9], v[34:49]
	v_mfma_f32_32x32x16_f16 v[2:17], v[70:73], v[126:129], 0
	s_nop 10
	v_cvt_pk_f16_f32 v41, v40, v41
	v_cvt_pk_f16_f32 v40, v38, v39
	v_cvt_pk_f16_f32 v38, v34, v35
	v_cvt_pk_f16_f32 v35, v44, v45
	v_cvt_pk_f16_f32 v34, v42, v43
	v_cvt_pk_f16_f32 v45, v32, v33
	v_cvt_pk_f16_f32 v44, v30, v31
	v_cvt_pk_f16_f32 v43, v28, v29
	v_cvt_pk_f16_f32 v42, v26, v27
	v_mfma_f32_32x32x16_f16 v[18:33], v[70:73], v[110:113], 0
	v_cvt_pk_f16_f32 v39, v36, v37
	v_cvt_pk_f16_f32 v37, v48, v49
	v_cvt_pk_f16_f32 v36, v46, v47
	ds_write_b128 v131, v[42:45]
	v_cvt_pk_f16_f32 v45, v56, v57
	v_cvt_pk_f16_f32 v44, v54, v55
	v_cvt_pk_f16_f32 v43, v52, v53
	v_mfma_f32_32x32x16_f16 v[2:17], v[66:69], v[122:125], v[2:17]
	v_cvt_pk_f16_f32 v42, v50, v51
	ds_write_b128 v132, v[42:45] offset:32768
	v_cvt_pk_f16_f32 v45, v64, v65
	v_cvt_pk_f16_f32 v44, v62, v63
	v_cvt_pk_f16_f32 v43, v60, v61
	v_cvt_pk_f16_f32 v42, v58, v59
	ds_write_b128 v131, v[42:45] offset:32768
	v_mfma_f32_32x32x16_f16 v[18:33], v[66:69], v[106:109], v[18:33]
	v_mfma_f32_32x32x16_f16 v[2:17], v[38:41], v[118:121], v[2:17]
	v_mfma_f32_32x32x16_f16 v[18:33], v[38:41], v[94:97], v[18:33]
	v_mfma_f32_32x32x16_f16 v[2:17], v[34:37], v[114:117], v[2:17]
	v_mfma_f32_32x32x16_f16 v[18:33], v[34:37], v[90:93], v[18:33]
	s_nop 10
	v_cvt_pk_f16_f32 v9, v8, v9
	v_cvt_pk_f16_f32 v8, v6, v7
	v_cvt_pk_f16_f32 v7, v4, v5
	v_cvt_pk_f16_f32 v6, v2, v3
	v_cvt_pk_f16_f32 v5, v16, v17
	v_cvt_pk_f16_f32 v4, v14, v15
	v_cvt_pk_f16_f32 v3, v12, v13
	v_cvt_pk_f16_f32 v2, v10, v11
	ds_write_b128 v135, v[6:9]
	ds_write_b128 v133, v[2:5]
	v_cvt_pk_f16_f32 v5, v24, v25
	v_cvt_pk_f16_f32 v4, v22, v23
	v_cvt_pk_f16_f32 v3, v20, v21
	v_cvt_pk_f16_f32 v2, v18, v19
	ds_write_b128 v135, v[2:5] offset:32768
	v_cvt_pk_f16_f32 v5, v32, v33
	v_cvt_pk_f16_f32 v4, v30, v31
	v_cvt_pk_f16_f32 v3, v28, v29
	v_cvt_pk_f16_f32 v2, v26, v27
	ds_write_b128 v133, v[2:5] offset:32768
	s_setprio 0
	s_waitcnt lgkmcnt(0)
	s_barrier
	ds_read_b64_tr_b16 v[2:3], v146
	ds_read_b64_tr_b16 v[4:5], v147
	ds_read_b64_tr_b16 v[36:37], v147 offset:32768
	ds_read_b64_tr_b16 v[34:35], v146 offset:32768
	ds_read_b64_tr_b16 v[18:19], v150
	ds_read_b64_tr_b16 v[20:21], v151
	ds_read_b64_tr_b16 v[40:41], v151 offset:32768
	ds_read_b64_tr_b16 v[38:39], v150 offset:32768
	s_waitcnt lgkmcnt(6)
	v_mfma_f32_32x32x16_f16 v[2:17], v[2:5], v[102:105], 0
	ds_read_b64_tr_b16 v[42:43], v148
	ds_read_b64_tr_b16 v[44:45], v149
	ds_read_b64_tr_b16 v[48:49], v149 offset:32768
	ds_read_b64_tr_b16 v[46:47], v148 offset:32768
	v_cmp_gt_u32_e64 s[0:1], 32, v167
	s_cmp_eq_u32 s5, 0
	v_cmp_lt_i32_e64 s[2:3], v162, v163
	s_waitcnt lgkmcnt(6)
	v_mfma_f32_32x32x16_f16 v[18:33], v[18:21], v[102:105], 0
	v_mfma_f32_32x32x16_f16 v[2:17], v[34:37], v[98:101], v[2:17]
	s_waitcnt lgkmcnt(4)
	v_mfma_f32_32x32x16_f16 v[18:33], v[38:41], v[98:101], v[18:33]
	s_nop 9
	v_mul_f32_e64 v34, v16, v16
	v_mul_f32_e64 v35, v17, v17
	v_mul_f32_e64 v36, v12, v12
	v_mul_f32_e64 v37, v13, v13
	v_mul_f32_e64 v50, v8, v8
	v_mul_f32_e64 v51, v9, v9
	v_pk_mul_f32 v[52:53], v[4:5], v[4:5]
	v_pk_fma_f32 v[50:51], v[6:7], v[6:7], v[50:51]
	v_pk_fma_f32 v[52:53], v[2:3], v[2:3], v[52:53]
	v_pk_fma_f32 v[36:37], v[10:11], v[10:11], v[36:37]
	v_pk_fma_f32 v[34:35], v[14:15], v[14:15], v[34:35]
	v_pk_mul_f32 v[116:117], v[24:25], v[24:25]
	v_pk_mul_f32 v[118:119], v[20:21], v[20:21]
	v_pk_add_f32 v[50:51], v[52:53], v[50:51]
	v_pk_add_f32 v[34:35], v[36:37], v[34:35]
	v_pk_mul_f32 v[112:113], v[32:33], v[32:33]
	v_pk_mul_f32 v[114:115], v[28:29], v[28:29]
	v_pk_mul_f32 v[120:121], v[18:19], v[18:19]
	v_pk_fma_f32 v[18:19], v[18:19], v[18:19], v[118:119]
	v_pk_fma_f32 v[20:21], v[22:23], v[22:23], v[116:117]
	v_pk_add_f32 v[34:35], v[50:51], v[34:35]
	v_pk_mul_f32 v[106:107], v[22:23], v[22:23]
	v_pk_add_f32 v[18:19], v[18:19], v[20:21]
	v_pk_fma_f32 v[20:21], v[26:27], v[26:27], v[114:115]
	v_pk_fma_f32 v[22:23], v[30:31], v[30:31], v[112:113]
	v_add_f32_e32 v34, v34, v35
	v_pk_add_f32 v[20:21], v[20:21], v[22:23]
	v_add_f32_e32 v36, 0, v34
	v_pk_mul_f32 v[108:109], v[26:27], v[26:27]
	v_pk_mul_f32 v[110:111], v[30:31], v[30:31]
	v_pk_add_f32 v[34:35], v[18:19], v[20:21]
	s_waitcnt lgkmcnt(2)
	v_mfma_f32_32x32x16_f16 v[18:33], v[42:45], v[102:105], 0
	v_add_f32_e32 v34, v34, v35
	v_add_f32_e32 v54, v36, v34
	v_sub_f32_e32 v55, v36, v34
	ds_read_b64_tr_b16 v[34:35], v144
	ds_read_b64_tr_b16 v[36:37], v145
	ds_read_b64_tr_b16 v[52:53], v145 offset:32768
	ds_read_b64_tr_b16 v[50:51], v144 offset:32768
	v_pk_fma_f32 v[4:5], v[4:5], v[4:5], v[118:119]
	v_pk_fma_f32 v[16:17], v[16:17], v[16:17], v[112:113]
	v_pk_fma_f32 v[14:15], v[14:15], v[14:15], v[110:111]
	s_waitcnt lgkmcnt(4)
	v_mfma_f32_32x32x16_f16 v[18:33], v[46:49], v[98:101], v[18:33]
	v_fma_f32 v12, v12, v12, v114
	v_fma_f32 v13, v13, v13, v115
	v_fma_f32 v10, v10, v10, v108
	v_fma_f32 v11, v11, v11, v109
	v_fma_f32 v8, v8, v8, v116
	v_fma_f32 v9, v9, v9, v117
	v_pk_fma_f32 v[6:7], v[6:7], v[6:7], v[106:107]
	v_pk_fma_f32 v[2:3], v[2:3], v[2:3], v[120:121]
	s_nop 3
	v_pk_mul_f32 v[38:39], v[32:33], v[32:33]
	v_pk_mul_f32 v[40:41], v[28:29], v[28:29]
	v_pk_mul_f32 v[42:43], v[24:25], v[24:25]
	v_pk_mul_f32 v[44:45], v[20:21], v[20:21]
	v_pk_fma_f32 v[42:43], v[22:23], v[22:23], v[42:43]
	v_pk_fma_f32 v[44:45], v[18:19], v[18:19], v[44:45]
	v_pk_fma_f32 v[40:41], v[26:27], v[26:27], v[40:41]
	v_pk_fma_f32 v[38:39], v[30:31], v[30:31], v[38:39]
	v_pk_add_f32 v[42:43], v[44:45], v[42:43]
	v_pk_add_f32 v[38:39], v[40:41], v[38:39]
	v_pk_fma_f32 v[4:5], v[20:21], v[20:21], v[4:5]
	v_pk_add_f32 v[38:39], v[42:43], v[38:39]
	v_pk_fma_f32 v[6:7], v[22:23], v[22:23], v[6:7]
	v_add_f32_e32 v56, v38, v39
	s_waitcnt lgkmcnt(2)
	v_mfma_f32_32x32x16_f16 v[34:49], v[34:37], v[102:105], 0
	v_add_f32_e32 v70, v54, v56
	v_add_f32_e32 v71, v55, v56
	v_sub_f32_e32 v72, v54, v56
	ds_read_b64_tr_b16 v[54:55], v142
	ds_read_b64_tr_b16 v[56:57], v143
	ds_read_b64_tr_b16 v[68:69], v143 offset:32768
	ds_read_b64_tr_b16 v[66:67], v142 offset:32768
	v_pk_fma_f32 v[8:9], v[24:25], v[24:25], v[8:9]
	v_pk_fma_f32 v[10:11], v[26:27], v[26:27], v[10:11]
	v_pk_fma_f32 v[12:13], v[28:29], v[28:29], v[12:13]
	s_waitcnt lgkmcnt(4)
	v_mfma_f32_32x32x16_f16 v[34:49], v[50:53], v[98:101], v[34:49]
	v_fma_f32 v14, v30, v30, v14
	v_fma_f32 v15, v31, v31, v15
	v_fma_f32 v16, v32, v32, v16
	v_fma_f32 v17, v33, v33, v17
	v_fma_f32 v2, v18, v18, v2
	v_fma_f32 v3, v19, v19, v3
	s_nop 5
	v_pk_mul_f32 v[50:51], v[48:49], v[48:49]
	v_pk_mul_f32 v[52:53], v[44:45], v[44:45]
	v_pk_mul_f32 v[58:59], v[40:41], v[40:41]
	v_pk_mul_f32 v[60:61], v[36:37], v[36:37]
	v_pk_fma_f32 v[58:59], v[38:39], v[38:39], v[58:59]
	v_pk_fma_f32 v[60:61], v[34:35], v[34:35], v[60:61]
	v_pk_fma_f32 v[52:53], v[42:43], v[42:43], v[52:53]
	v_pk_fma_f32 v[50:51], v[46:47], v[46:47], v[50:51]
	v_pk_add_f32 v[58:59], v[60:61], v[58:59]
	v_pk_add_f32 v[50:51], v[52:53], v[50:51]
	v_pk_fma_f32 v[4:5], v[36:37], v[36:37], v[4:5]
	v_pk_add_f32 v[50:51], v[58:59], v[50:51]
	v_pk_fma_f32 v[16:17], v[48:49], v[48:49], v[16:17]
	v_add_f32_e32 v73, v50, v51
	s_waitcnt lgkmcnt(2)
	v_mfma_f32_32x32x16_f16 v[50:65], v[54:57], v[102:105], 0
	v_add_f32_e32 v86, v70, v73
	v_sub_f32_e32 v87, v71, v73
	v_sub_f32_e32 v88, v72, v73
	ds_read_b64_tr_b16 v[70:71], v140
	ds_read_b64_tr_b16 v[72:73], v141
	ds_read_b64_tr_b16 v[84:85], v141 offset:32768
	ds_read_b64_tr_b16 v[82:83], v140 offset:32768
	v_pk_fma_f32 v[14:15], v[46:47], v[46:47], v[14:15]
	v_pk_fma_f32 v[12:13], v[44:45], v[44:45], v[12:13]
	v_pk_fma_f32 v[10:11], v[42:43], v[42:43], v[10:11]
	s_waitcnt lgkmcnt(4)
	v_mfma_f32_32x32x16_f16 v[50:65], v[66:69], v[98:101], v[50:65]
	v_fma_f32 v8, v40, v40, v8
	v_fma_f32 v9, v41, v41, v9
	v_fma_f32 v6, v38, v38, v6
	v_fma_f32 v7, v39, v39, v7
	v_fma_f32 v2, v34, v34, v2
	v_fma_f32 v3, v35, v35, v3
	s_nop 5
	v_pk_mul_f32 v[66:67], v[64:65], v[64:65]
	v_pk_mul_f32 v[68:69], v[60:61], v[60:61]
	v_pk_mul_f32 v[74:75], v[56:57], v[56:57]
	v_pk_mul_f32 v[76:77], v[52:53], v[52:53]
	v_pk_fma_f32 v[74:75], v[54:55], v[54:55], v[74:75]
	v_pk_fma_f32 v[76:77], v[50:51], v[50:51], v[76:77]
	v_pk_fma_f32 v[68:69], v[58:59], v[58:59], v[68:69]
	v_pk_fma_f32 v[66:67], v[62:63], v[62:63], v[66:67]
	v_pk_add_f32 v[74:75], v[76:77], v[74:75]
	v_pk_add_f32 v[66:67], v[68:69], v[66:67]
	v_pk_fma_f32 v[4:5], v[52:53], v[52:53], v[4:5]
	v_pk_add_f32 v[66:67], v[74:75], v[66:67]
	v_pk_fma_f32 v[6:7], v[54:55], v[54:55], v[6:7]
	v_add_f32_e32 v89, v66, v67
	s_waitcnt lgkmcnt(2)
	v_mfma_f32_32x32x16_f16 v[66:81], v[70:73], v[102:105], 0
	v_add_f32_e32 v94, v86, v89
	v_add_f32_e32 v126, v87, v89
	v_add_f32_e32 v127, v88, v89
	v_sub_f32_e32 v128, v86, v89
	ds_read_b64_tr_b16 v[86:87], v138
	ds_read_b64_tr_b16 v[88:89], v139
	ds_read_b64_tr_b16 v[124:125], v139 offset:32768
	ds_read_b64_tr_b16 v[122:123], v138 offset:32768
	v_pk_fma_f32 v[8:9], v[56:57], v[56:57], v[8:9]
	v_pk_fma_f32 v[10:11], v[58:59], v[58:59], v[10:11]
	s_waitcnt lgkmcnt(4)
	v_mfma_f32_32x32x16_f16 v[66:81], v[82:85], v[98:101], v[66:81]
	v_fma_f32 v12, v60, v60, v12
	v_fma_f32 v13, v61, v61, v13
	v_fma_f32 v14, v62, v62, v14
	v_fma_f32 v15, v63, v63, v15
	v_fma_f32 v16, v64, v64, v16
	v_fma_f32 v17, v65, v65, v17
	v_pk_fma_f32 v[2:3], v[50:51], v[50:51], v[2:3]
	s_nop 4
	v_pk_mul_f32 v[82:83], v[80:81], v[80:81]
	v_pk_mul_f32 v[84:85], v[76:77], v[76:77]
	v_pk_mul_f32 v[90:91], v[72:73], v[72:73]
	v_pk_mul_f32 v[92:93], v[68:69], v[68:69]
	v_pk_fma_f32 v[90:91], v[70:71], v[70:71], v[90:91]
	v_pk_fma_f32 v[92:93], v[66:67], v[66:67], v[92:93]
	v_pk_fma_f32 v[84:85], v[74:75], v[74:75], v[84:85]
	v_pk_fma_f32 v[82:83], v[78:79], v[78:79], v[82:83]
	v_pk_add_f32 v[90:91], v[92:93], v[90:91]
	v_pk_add_f32 v[82:83], v[84:85], v[82:83]
	v_pk_fma_f32 v[4:5], v[68:69], v[68:69], v[4:5]
	v_pk_add_f32 v[82:83], v[90:91], v[82:83]
	v_pk_fma_f32 v[18:19], v[80:81], v[80:81], v[16:17]
	v_add_f32_e32 v129, v82, v83
	v_add_f32_e32 v131, v94, v129
	s_waitcnt lgkmcnt(2)
	v_mfma_f32_32x32x16_f16 v[82:97], v[86:89], v[102:105], 0
	v_sub_f32_e32 v135, v126, v129
	v_add_f32_e32 v142, v127, v129
	v_sub_f32_e32 v143, v128, v129
	ds_read_b64_tr_b16 v[126:127], v136
	ds_read_b64_tr_b16 v[128:129], v137
	ds_read_b64_tr_b16 v[138:139], v137 offset:32768
	ds_read_b64_tr_b16 v[136:137], v136 offset:32768
	v_pk_fma_f32 v[20:21], v[78:79], v[78:79], v[14:15]
	v_pk_fma_f32 v[22:23], v[76:77], v[76:77], v[12:13]
	v_pk_fma_f32 v[24:25], v[74:75], v[74:75], v[10:11]
	s_waitcnt lgkmcnt(4)
	v_mfma_f32_32x32x16_f16 v[82:97], v[122:125], v[98:101], v[82:97]
	v_fma_f32 v26, v72, v72, v8
	v_fma_f32 v27, v73, v73, v9
	v_fma_f32 v28, v70, v70, v6
	v_fma_f32 v29, v71, v71, v7
	v_fma_f32 v30, v66, v66, v2
	v_fma_f32 v31, v67, v67, v3
	s_nop 5
	v_pk_fma_f32 v[32:33], v[84:85], v[84:85], v[4:5]
	s_waitcnt lgkmcnt(2)
	v_mfma_f32_32x32x16_f16 v[2:17], v[126:129], v[102:105], 0
	v_fma_f32 v28, v86, v86, v28
	v_fma_f32 v29, v87, v87, v29
	v_fma_f32 v24, v90, v90, v24
	v_fma_f32 v25, v91, v91, v25
	v_fma_f32 v22, v92, v92, v22
	v_fma_f32 v23, v93, v93, v23
	v_pk_fma_f32 v[20:21], v[94:95], v[94:95], v[20:21]
	v_pk_fma_f32 v[18:19], v[96:97], v[96:97], v[18:19]
	v_pk_fma_f32 v[30:31], v[82:83], v[82:83], v[30:31]
	v_pk_fma_f32 v[26:27], v[88:89], v[88:89], v[26:27]
	s_waitcnt lgkmcnt(0)
	v_mfma_f32_32x32x16_f16 v[2:17], v[136:139], v[98:101], v[2:17]
	v_mul_f32_e64 v122, v96, v96
	v_mul_f32_e64 v123, v97, v97
	v_mul_f32_e64 v124, v92, v92
	v_mul_f32_e64 v125, v93, v93
	v_mul_f32_e64 v132, v88, v88
	v_mul_f32_e64 v133, v89, v89
	v_pk_mul_f32 v[140:141], v[84:85], v[84:85]
	v_pk_fma_f32 v[132:133], v[86:87], v[86:87], v[132:133]
	v_pk_fma_f32 v[140:141], v[82:83], v[82:83], v[140:141]
	v_pk_fma_f32 v[124:125], v[90:91], v[90:91], v[124:125]
	s_nop 1
	v_pk_mul_f32 v[38:39], v[8:9], v[8:9]
	v_pk_mul_f32 v[40:41], v[4:5], v[4:5]
	v_pk_mul_f32 v[34:35], v[16:17], v[16:17]
	v_pk_mul_f32 v[36:37], v[12:13], v[12:13]
	v_pk_fma_f32 v[16:17], v[16:17], v[16:17], v[18:19]
	v_pk_fma_f32 v[18:19], v[14:15], v[14:15], v[20:21]
	v_pk_fma_f32 v[12:13], v[12:13], v[12:13], v[22:23]
	v_pk_fma_f32 v[20:21], v[10:11], v[10:11], v[24:25]
	v_pk_fma_f32 v[22:23], v[6:7], v[6:7], v[28:29]
	v_pk_fma_f32 v[24:25], v[2:3], v[2:3], v[30:31]
	v_pk_fma_f32 v[2:3], v[2:3], v[2:3], v[40:41]
	v_pk_fma_f32 v[6:7], v[6:7], v[6:7], v[38:39]
	v_pk_fma_f32 v[4:5], v[4:5], v[4:5], v[32:33]
	v_pk_add_f32 v[2:3], v[2:3], v[6:7]
	v_pk_fma_f32 v[6:7], v[10:11], v[10:11], v[36:37]
	v_pk_fma_f32 v[10:11], v[14:15], v[14:15], v[34:35]
	v_pk_fma_f32 v[8:9], v[8:9], v[8:9], v[26:27]
	v_pk_add_f32 v[6:7], v[6:7], v[10:11]
	v_sub_f32_e32 v10, v24, v25
	v_add_f32_e32 v11, v25, v24
	v_add_f32_e32 v10, v4, v10
	v_sub_f32_e32 v14, v11, v4
	v_add_f32_e32 v4, v4, v11
	v_sub_f32_e32 v10, v10, v5
	v_sub_f32_e32 v11, v14, v5
	v_add_f32_e32 v4, v5, v4
	v_add_f32_e32 v5, v22, v10
	v_add_f32_e32 v10, v22, v11
	v_sub_f32_e32 v11, v4, v22
	v_add_f32_e32 v4, v22, v4
	v_sub_f32_e32 v5, v5, v23
	v_add_f32_e32 v10, v23, v10
	v_sub_f32_e32 v11, v11, v23
	v_add_f32_e32 v4, v23, v4
	v_add_f32_e32 v5, v8, v5
	v_sub_f32_e32 v10, v10, v8
	v_sub_f32_e32 v11, v11, v8
	v_add_f32_e32 v4, v8, v4
	v_sub_f32_e32 v5, v5, v9
	v_pk_fma_f32 v[122:123], v[94:95], v[94:95], v[122:123]
	v_sub_f32_e32 v8, v10, v9
	v_sub_f32_e32 v10, v11, v9
	v_add_f32_e32 v4, v9, v4
	v_add_f32_e32 v5, v20, v5
	v_pk_add_f32 v[132:133], v[140:141], v[132:133]
	v_pk_add_f32 v[122:123], v[124:125], v[122:123]
	v_add_f32_e32 v8, v20, v8
	v_add_f32_e32 v9, v20, v10
	v_sub_f32_e32 v4, v4, v20
	v_sub_f32_e32 v5, v5, v21
	v_pk_add_f32 v[122:123], v[132:133], v[122:123]
	v_add_f32_e32 v8, v21, v8
	v_add_f32_e32 v9, v21, v9
	v_sub_f32_e32 v4, v4, v21
	v_add_f32_e32 v5, v12, v5
	v_add_f32_e32 v122, v122, v123
	v_pk_add_f32 v[2:3], v[2:3], v[6:7]
	v_sub_f32_e32 v8, v8, v12
	v_add_f32_e32 v9, v12, v9
	v_sub_f32_e32 v4, v4, v12
	v_sub_f32_e32 v5, v5, v13
	v_add_f32_e32 v123, v131, v122
	v_add_f32_e32 v2, v2, v3
	v_sub_f32_e32 v8, v8, v13
	v_add_f32_e32 v9, v13, v9
	v_sub_f32_e32 v4, v4, v13
	v_add_f32_e32 v5, v18, v5
	v_add_f32_e32 v3, v123, v2
	v_add_f32_e32 v8, v18, v8
	v_sub_f32_e32 v9, v9, v18
	v_sub_f32_e32 v4, v4, v18
	v_sub_f32_e32 v5, v5, v19
	v_and_b32_e32 v10, 8, v156
	v_add_f32_e32 v8, v19, v8
	v_sub_f32_e32 v9, v9, v19
	v_sub_f32_e32 v4, v4, v19
	v_add_f32_e32 v5, v16, v5
	v_cmp_eq_u32_e32 vcc, 0, v10
	v_cndmask_b32_e64 v10, -v3, v3, s[0:1]
	s_cselect_b64 s[0:1], -1, 0
	s_bitcmp0_b32 s4, 7
	v_sub_f32_e32 v8, v8, v16
	v_sub_f32_e32 v9, v9, v16
	v_sub_f32_e32 v4, v4, v16
	v_sub_f32_e32 v5, v5, v17
	v_cndmask_b32_e64 v11, -v3, v3, s[0:1]
	s_cselect_b64 s[0:1], -1, 0
	v_and_b32_e32 v16, 32, v156
	v_sub_f32_e32 v8, v8, v17
	v_cndmask_b32_e64 v5, -v5, v5, vcc
	v_cndmask_b32_e64 v12, -v3, v3, s[0:1]
	v_cndmask_b32_e64 v18, v161, v162, s[2:3]
	v_cmp_eq_u32_e64 s[2:3], 0, v16
	v_lshlrev_b32_e32 v18, 2, v18
	v_cmp_eq_u32_e64 s[0:1], 0, v134
	v_cndmask_b32_e64 v16, v11, v5, s[2:3]
	v_cndmask_b32_e64 v5, v5, v11, s[2:3]
	v_cndmask_b32_e64 v11, v8, v12, s[2:3]
	ds_bpermute_b32 v11, v18, v11
	v_and_b32_e32 v14, 2, v156
	v_cndmask_b32_e64 v13, -v3, v3, s[0:1]
	v_cmp_eq_u32_e64 s[0:1], 0, v14
	v_cndmask_b32_e64 v8, v12, v8, s[2:3]
	v_add_f32_e32 v124, v135, v122
	v_cndmask_b32_e64 v14, -v3, v3, s[0:1]
	v_cmp_eq_u32_e64 s[0:1], 0, v130
	v_sub_f32_e32 v4, v4, v17
	s_waitcnt lgkmcnt(0)
	v_add_f32_e32 v8, v8, v11
	v_cndmask_b32_e64 v15, -v3, v3, s[0:1]
	v_cndmask_b32_e64 v11, v14, v10, s[2:3]
	v_cndmask_b32_e64 v10, v10, v14, s[2:3]
	v_sub_f32_e32 v6, v124, v2
	v_sub_f32_e32 v9, v9, v17
	v_cndmask_b32_e64 v3, -v3, v3, vcc
	ds_bpermute_b32 v10, v18, v10
	v_cndmask_b32_e64 v12, v4, v15, s[2:3]
	v_sub_f32_e32 v125, v142, v122
	v_cndmask_b32_e64 v19, v9, v13, s[2:3]
	v_cndmask_b32_e64 v9, v13, v9, s[2:3]
	ds_bpermute_b32 v12, v18, v12
	v_cndmask_b32_e64 v13, v6, v3, s[2:3]
	v_sub_f32_e32 v7, v125, v2
	v_bfe_i32 v17, v156, 5, 1
	ds_bpermute_b32 v5, v18, v5
	ds_bpermute_b32 v13, v18, v13
	v_sub_f32_e32 v122, v143, v122
	v_cndmask_b32_e64 v3, v3, v6, s[2:3]
	v_and_b32_e32 v6, v17, v7
	v_sub_f32_e32 v2, v122, v2
	ds_bpermute_b32 v19, v18, v19
	ds_bpermute_b32 v6, v18, v6
	s_waitcnt lgkmcnt(5)
	v_add_f32_e32 v10, v11, v10
	v_cndmask_b32_e64 v4, v15, v4, s[2:3]
	v_and_b32_e32 v11, v17, v2
	s_waitcnt lgkmcnt(4)
	v_add_f32_e32 v4, v4, v12
	ds_bpermute_b32 v11, v18, v11
	v_and_b32_e32 v12, 16, v156
	v_cmp_lt_i32_e64 s[4:5], v164, v163
	s_waitcnt lgkmcnt(4)
	v_add_f32_e32 v5, v16, v5
	s_waitcnt lgkmcnt(3)
	v_add_f32_e32 v3, v3, v13
	v_cndmask_b32_e64 v13, v161, v164, s[4:5]
	v_cmp_eq_u32_e64 s[4:5], 0, v12
	s_waitcnt lgkmcnt(2)
	v_add_f32_e32 v9, v9, v19
	v_lshlrev_b32_e32 v13, 2, v13
	v_cndmask_b32_e64 v12, v4, v5, s[4:5]
	v_cndmask_b32_e64 v4, v5, v4, s[4:5]
	v_cndmask_b32_e64 v5, 0, v7, s[2:3]
	s_waitcnt lgkmcnt(1)
	v_add_f32_e32 v5, v5, v6
	v_cndmask_b32_e64 v2, 0, v2, s[2:3]
	v_cndmask_b32_e64 v7, v9, v5, s[4:5]
	ds_bpermute_b32 v4, v13, v4
	s_waitcnt lgkmcnt(1)
	v_add_f32_e32 v2, v2, v11
	v_cndmask_b32_e64 v6, v3, v8, s[4:5]
	v_cndmask_b32_e64 v3, v8, v3, s[4:5]
	ds_bpermute_b32 v7, v13, v7
	ds_bpermute_b32 v3, v13, v3
	v_cndmask_b32_e64 v8, v10, v2, s[4:5]
	ds_bpermute_b32 v8, v13, v8
	v_cndmask_b32_e64 v5, v5, v9, s[4:5]
	s_waitcnt lgkmcnt(3)
	v_add_f32_e32 v4, v12, v4
	s_waitcnt lgkmcnt(2)
	v_add_f32_e32 v5, v5, v7
	s_waitcnt lgkmcnt(1)
	v_add_f32_e32 v3, v6, v3
	v_cndmask_b32_e64 v2, v2, v10, s[4:5]
	v_cndmask_b32_e32 v6, v5, v4, vcc
	v_cndmask_b32_e32 v4, v4, v5, vcc
	v_mov_b32_e32 v5, v155
	s_waitcnt lgkmcnt(0)
	v_add_f32_e32 v2, v2, v8
	v_mov_b32_dpp v5, v4 row_mirror row_mask:0xf bank_mask:0xf
	s_nop 1
	v_add_f32_dpp v4, v5, v6 row_half_mirror row_mask:0xf bank_mask:0xf bound_ctrl:1
	v_cndmask_b32_e32 v5, v2, v3, vcc
	v_cndmask_b32_e32 v2, v3, v2, vcc
	v_mov_b32_e32 v3, v155
	s_nop 1
	v_mov_b32_dpp v3, v2 row_mirror row_mask:0xf bank_mask:0xf
	s_nop 1
	v_add_f32_dpp v2, v3, v5 row_half_mirror row_mask:0xf bank_mask:0xf bound_ctrl:1
	v_cndmask_b32_e64 v3, v2, v4, s[0:1]
	v_cndmask_b32_e64 v2, v4, v2, s[0:1]
	v_mov_b32_e32 v4, v155
	s_nop 1
	v_mov_b32_dpp v4, v2 row_half_mirror row_mask:0xf bank_mask:0xf
	s_nop 1
	v_add_f32_dpp v2, v4, v3 quad_perm:[3,2,1,0] row_mask:0xf bank_mask:0xf bound_ctrl:1
	v_and_b32_e32 v4, 3, v156
	v_cmp_eq_u32_e32 vcc, 0, v4
	v_and_b32_e32 v4, 56, v156
	v_add_f32_dpp v2, v2, v2 quad_perm:[2,3,0,1] row_mask:0xf bank_mask:0xf bound_ctrl:1
	v_mov_b32_e32 v3, 0
	v_cmp_ne_u32_e64 s[0:1], 56, v4
	s_and_b64 s[2:3], vcc, s[0:1]
	v_mov_b32_dpp v3, v2 quad_perm:[1,0,3,2] row_mask:0xf bank_mask:0xf
	s_and_saveexec_b64 s[0:1], s[2:3]
	v_and_b32_e32 v4, 0xfc, v156
	v_add_f32_e32 v2, v2, v3
	v_or_b32_e32 v4, v165, v4
	ds_write_b32 v4, v2
	s_or_b64 exec, exec, s[0:1]
	v_cmp_gt_i32_e32 vcc, 14, v156
	s_waitcnt lgkmcnt(0)
	s_barrier
	s_and_saveexec_b64 s[0:1], vcc
	s_cbranch_execz .LBB1_2
	ds_read_b32 v2, v166
	ds_read_b32 v3, v166 offset:64
	ds_read_b32 v4, v166 offset:128
	ds_read_b32 v5, v166 offset:192
	s_waitcnt lgkmcnt(2)
	v_add_f32_e32 v2, v2, v3
	s_waitcnt lgkmcnt(1)
	v_add_f32_e32 v2, v2, v4
	s_waitcnt lgkmcnt(0)
	v_add_f32_e32 v2, v2, v5
	v_mul_f32_e32 v4, 0x39800000, v2
	v_lshl_add_u64 v[2:3], v[156:157], 2, s[14:15]
	global_store_dword v[2:3], v4, off
	s_branch .LBB1_2

	.amdhsa_kernel _Z9qsim_mainPKDF16_PK15HIP_vector_typeIfLj2EEPf
		.amdhsa_group_segment_fixed_size 68352
		.amdhsa_private_segment_fixed_size 0
		.amdhsa_kernarg_size 24
		.amdhsa_user_sgpr_count 2
		.amdhsa_user_sgpr_dispatch_ptr 0
		.amdhsa_user_sgpr_queue_ptr 0
		.amdhsa_user_sgpr_kernarg_segment_ptr 1
		.amdhsa_user_sgpr_dispatch_id 0
		.amdhsa_user_sgpr_kernarg_preload_length 0
		.amdhsa_user_sgpr_kernarg_preload_offset 0
		.amdhsa_user_sgpr_private_segment_size 0
		.amdhsa_uses_dynamic_stack 0
		.amdhsa_enable_private_segment 0
		.amdhsa_system_sgpr_workgroup_id_x 1
		.amdhsa_system_sgpr_workgroup_id_y 0
		.amdhsa_system_sgpr_workgroup_id_z 0
		.amdhsa_system_sgpr_workgroup_info 0
		.amdhsa_system_vgpr_workitem_id 0
		.amdhsa_next_free_vgpr 256
		.amdhsa_next_free_sgpr 96
		.amdhsa_accum_offset 256
		.amdhsa_reserve_vcc 1
		.amdhsa_float_round_mode_32 0
		.amdhsa_float_round_mode_16_64 0
		.amdhsa_float_denorm_mode_32 3
		.amdhsa_float_denorm_mode_16_64 3
		.amdhsa_dx10_clamp 1
		.amdhsa_ieee_mode 1
		.amdhsa_fp16_overflow 0
		.amdhsa_tg_split 0
		.amdhsa_exception_fp_ieee_invalid_op 0
		.amdhsa_exception_fp_denorm_src 0
		.amdhsa_exception_fp_ieee_div_zero 0
		.amdhsa_exception_fp_ieee_overflow 0
		.amdhsa_exception_fp_ieee_underflow 0
		.amdhsa_exception_fp_ieee_inexact 0
		.amdhsa_exception_int_div_zero 0
	.end_amdhsa_kernel

amdhsa.kernels:
  - .agpr_count:     0
    .args:
      - .actual_access:  read_only
        .address_space:  global
        .offset:         0
        .size:           8
        .value_kind:     global_buffer
      - .actual_access:  read_only
        .address_space:  global
        .offset:         8
        .size:           8
        .value_kind:     global_buffer
      - .actual_access:  read_only
        .address_space:  global
        .offset:         16
        .size:           8
        .value_kind:     global_buffer
      - .actual_access:  read_only
        .address_space:  global
        .offset:         24
        .size:           8
        .value_kind:     global_buffer
      - .actual_access:  write_only
        .address_space:  global
        .offset:         32
        .size:           8
        .value_kind:     global_buffer
      - .actual_access:  write_only
        .address_space:  global
        .offset:         40
        .size:           8
        .value_kind:     global_buffer
    .group_segment_fixed_size: 1920
    .kernarg_segment_align: 8
    .kernarg_segment_size: 48
    .language:       OpenCL C
    .language_version:
      - 2
      - 0
    .max_flat_workgroup_size: 256
    .name:           _Z11prep_kernelPKfS0_S0_S0_PDF16_P15HIP_vector_typeIfLj2EE
    .private_segment_fixed_size: 0
    .sgpr_count:     22
    .sgpr_spill_count: 0
    .symbol:         _Z11prep_kernelPKfS0_S0_S0_PDF16_P15HIP_vector_typeIfLj2EE.kd
    .uniform_work_group_size: 1
    .uses_dynamic_stack: false
    .vgpr_count:     59
    .vgpr_spill_count: 0
    .wavefront_size: 64
  - .agpr_count:     0
    .args:
      - .actual_access:  read_only
        .address_space:  global
        .offset:         0
        .size:           8
        .value_kind:     global_buffer
      - .actual_access:  read_only
        .address_space:  global
        .offset:         8
        .size:           8
        .value_kind:     global_buffer
      - .actual_access:  write_only
        .address_space:  global
        .offset:         16
        .size:           8
        .value_kind:     global_buffer
    .group_segment_fixed_size: 68352
    .kernarg_segment_align: 8
    .kernarg_segment_size: 24
    .language:       OpenCL C
    .language_version:
      - 2
      - 0
    .max_flat_workgroup_size: 256
    .name:           _Z9qsim_mainPKDF16_PK15HIP_vector_typeIfLj2EEPf
    .private_segment_fixed_size: 0
    .sgpr_count:     41
    .sgpr_spill_count: 0
    .symbol:         _Z9qsim_mainPKDF16_PK15HIP_vector_typeIfLj2EEPf.kd
    .uniform_work_group_size: 1
    .uses_dynamic_stack: false
    .vgpr_count:     256
    .vgpr_spill_count: 0
    .wavefront_size: 64
